# GEMM loops: the 12 address computations of the two 6-DMA load segments hoisted into the preceding MFMA blocks (fresh VGPR pairs), so those near-critical load segments carry no VALU; on top of v024
# baseline (speedup 1.0000x reference)
.LBB0_261:
	ds_read_b128 v[144:147], v170
	ds_read_b128 v[148:151], v170 offset:1024
	ds_read_b128 v[174:177], v170 offset:2048
	ds_read_b128 v[178:181], v170 offset:3072
	ds_read_b128 v[182:185], v171
	ds_read_b128 v[186:189], v171 offset:1024
	ds_read_b128 v[190:193], v171 offset:2048
	ds_read_b128 v[194:197], v171 offset:3072
	s_add_u32 s26, s80, 0xfff80080
	s_addc_u32 s27, s81, -1
	s_cmp_eq_u32 vcc_hi, 28
	s_cselect_b32 s83, s69, s27
	s_cselect_b32 s82, s75, s26
	s_cselect_b32 s27, s57, vcc_lo
	s_cselect_b32 s26, s96, s97
	v_lshl_add_u64 v[152:153], s[80:81], 0, v[134:135]
	s_add_i32 m0, s87, 0xc000
	ds_read_b128 v[198:201], v172
	ds_read_b128 v[202:205], v172 offset:1024
	ds_read_b128 v[206:209], v172 offset:2048
	ds_read_b128 v[210:213], v172 offset:3072
	ds_read_b128 v[214:217], v172 offset:4096
	ds_read_b128 v[220:223], v172 offset:5120
	ds_read_b128 v[224:227], v172 offset:6144
	ds_read_b128 v[228:231], v172 offset:7168
	global_load_lds_dwordx4 v[152:153], off
	v_lshl_add_u64 v[152:153], s[80:81], 0, v[138:139]
	s_add_i32 m0, s87, 0xe000
	s_nop 0
	global_load_lds_dwordx4 v[152:153], off
	s_waitcnt vmcnt(8)
	s_waitcnt lgkmcnt(0)
	s_barrier
	s_waitcnt lgkmcnt(0)
	v_mfma_f32_16x16x32_bf16 v[122:125], v[144:147], v[198:201], v[122:125]
	v_mfma_f32_16x16x32_bf16 v[118:121], v[174:177], v[198:201], v[118:121]
	v_lshl_add_u64 v[240:241], s[26:27], 0, v[162:163]
	v_mfma_f32_16x16x32_bf16 v[106:109], v[144:147], v[206:209], v[106:109]
	v_mfma_f32_16x16x32_bf16 v[102:105], v[174:177], v[206:209], v[102:105]
	v_lshl_add_u64 v[242:243], v[240:241], 0, s[10:11]
	v_mfma_f32_16x16x32_bf16 v[90:93], v[144:147], v[214:217], v[90:93]
	v_mfma_f32_16x16x32_bf16 v[86:89], v[174:177], v[214:217], v[86:89]
	v_lshl_add_u64 v[244:245], v[240:241], 0, s[12:13]
	v_mfma_f32_16x16x32_bf16 v[74:77], v[144:147], v[224:227], v[74:77]
	v_mfma_f32_16x16x32_bf16 v[70:73], v[174:177], v[224:227], v[70:73]
	v_lshl_add_u64 v[246:247], s[82:83], 0, v[132:133]
	v_mfma_f32_16x16x32_bf16 v[122:125], v[148:151], v[202:205], v[122:125]
	v_mfma_f32_16x16x32_bf16 v[118:121], v[178:181], v[202:205], v[118:121]
	v_lshl_add_u64 v[248:249], v[240:241], 0, s[14:15]
	v_mfma_f32_16x16x32_bf16 v[106:109], v[148:151], v[210:213], v[106:109]
	v_mfma_f32_16x16x32_bf16 v[102:105], v[178:181], v[210:213], v[102:105]
	v_lshl_add_u64 v[250:251], s[82:83], 0, v[130:131]
	v_mfma_f32_16x16x32_bf16 v[90:93], v[148:151], v[220:223], v[90:93]
	v_mfma_f32_16x16x32_bf16 v[86:89], v[178:181], v[220:223], v[86:89]
	v_mfma_f32_16x16x32_bf16 v[74:77], v[148:151], v[228:231], v[74:77]
	v_mfma_f32_16x16x32_bf16 v[70:73], v[178:181], v[228:231], v[70:73]
	v_mfma_f32_16x16x32_bf16 v[126:129], v[182:185], v[198:201], v[126:129]
	v_mfma_f32_16x16x32_bf16 v[114:117], v[190:193], v[198:201], v[114:117]
	v_mfma_f32_16x16x32_bf16 v[110:113], v[182:185], v[206:209], v[110:113]
	v_mfma_f32_16x16x32_bf16 v[98:101], v[190:193], v[206:209], v[98:101]
	v_mfma_f32_16x16x32_bf16 v[94:97], v[182:185], v[214:217], v[94:97]
	v_mfma_f32_16x16x32_bf16 v[82:85], v[190:193], v[214:217], v[82:85]
	v_mfma_f32_16x16x32_bf16 v[78:81], v[182:185], v[224:227], v[78:81]
	v_mfma_f32_16x16x32_bf16 v[66:69], v[190:193], v[224:227], v[66:69]
	v_mfma_f32_16x16x32_bf16 v[126:129], v[186:189], v[202:205], v[126:129]
	v_mfma_f32_16x16x32_bf16 v[114:117], v[194:197], v[202:205], v[114:117]
	v_mfma_f32_16x16x32_bf16 v[110:113], v[186:189], v[210:213], v[110:113]
	v_mfma_f32_16x16x32_bf16 v[98:101], v[194:197], v[210:213], v[98:101]
	v_mfma_f32_16x16x32_bf16 v[94:97], v[186:189], v[220:223], v[94:97]
	v_mfma_f32_16x16x32_bf16 v[82:85], v[194:197], v[220:223], v[82:85]
	v_mfma_f32_16x16x32_bf16 v[78:81], v[186:189], v[228:231], v[78:81]
	v_mfma_f32_16x16x32_bf16 v[66:69], v[194:197], v[228:231], v[66:69]
	s_barrier
	s_add_i32 s26, s94, s86
	s_mov_b32 m0, s26
	ds_read_b128 v[198:201], v172 offset:16384
	ds_read_b128 v[202:205], v172 offset:17408
	ds_read_b128 v[206:209], v172 offset:18432
	ds_read_b128 v[210:213], v172 offset:19456
	ds_read_b128 v[214:217], v172 offset:20480
	ds_read_b128 v[220:223], v172 offset:21504
	ds_read_b128 v[224:227], v172 offset:22528
	ds_read_b128 v[228:231], v172 offset:23552
	global_load_lds_dwordx4 v[240:241], off
	s_add_i32 m0, s26, 0x2000
	s_add_i32 s26, s95, s86
	global_load_lds_dwordx4 v[242:243], off
	s_mov_b32 m0, s26
	s_nop 0
	global_load_lds_dwordx4 v[244:245], off
	s_add_i32 m0, s26, 0x2000
	s_nop 0
	global_load_lds_dwordx4 v[248:249], off
	s_mov_b32 m0, s87
	s_nop 0
	global_load_lds_dwordx4 v[250:251], off
	s_mov_b32 m0, s88
	s_nop 0
	global_load_lds_dwordx4 v[246:247], off
	s_waitcnt vmcnt(8)
	s_waitcnt lgkmcnt(0)
	s_barrier
	s_waitcnt lgkmcnt(0)
	v_mfma_f32_16x16x32_bf16 v[58:61], v[144:147], v[198:201], v[58:61]
	v_mfma_f32_16x16x32_bf16 v[54:57], v[174:177], v[198:201], v[54:57]
	v_mfma_f32_16x16x32_bf16 v[42:45], v[144:147], v[206:209], v[42:45]
	v_mfma_f32_16x16x32_bf16 v[38:41], v[174:177], v[206:209], v[38:41]
	v_mfma_f32_16x16x32_bf16 v[26:29], v[144:147], v[214:217], v[26:29]
	v_mfma_f32_16x16x32_bf16 v[22:25], v[174:177], v[214:217], v[22:25]
	v_mfma_f32_16x16x32_bf16 v[10:13], v[144:147], v[224:227], v[10:13]
	v_mfma_f32_16x16x32_bf16 v[6:9], v[174:177], v[224:227], v[6:9]
	v_mfma_f32_16x16x32_bf16 v[58:61], v[148:151], v[202:205], v[58:61]
	v_mfma_f32_16x16x32_bf16 v[54:57], v[178:181], v[202:205], v[54:57]
	v_mfma_f32_16x16x32_bf16 v[42:45], v[148:151], v[210:213], v[42:45]
	v_mfma_f32_16x16x32_bf16 v[38:41], v[178:181], v[210:213], v[38:41]
	v_mfma_f32_16x16x32_bf16 v[26:29], v[148:151], v[220:223], v[26:29]
	v_mfma_f32_16x16x32_bf16 v[22:25], v[178:181], v[220:223], v[22:25]
	v_mfma_f32_16x16x32_bf16 v[10:13], v[148:151], v[228:231], v[10:13]
	v_mfma_f32_16x16x32_bf16 v[6:9], v[178:181], v[228:231], v[6:9]
	v_mfma_f32_16x16x32_bf16 v[62:65], v[182:185], v[198:201], v[62:65]
	v_mfma_f32_16x16x32_bf16 v[50:53], v[190:193], v[198:201], v[50:53]
	v_mfma_f32_16x16x32_bf16 v[46:49], v[182:185], v[206:209], v[46:49]
	v_mfma_f32_16x16x32_bf16 v[34:37], v[190:193], v[206:209], v[34:37]
	v_mfma_f32_16x16x32_bf16 v[30:33], v[182:185], v[214:217], v[30:33]
	v_mfma_f32_16x16x32_bf16 v[18:21], v[190:193], v[214:217], v[18:21]
	v_mfma_f32_16x16x32_bf16 v[14:17], v[182:185], v[224:227], v[14:17]
	v_mfma_f32_16x16x32_bf16 v[2:5], v[190:193], v[224:227], v[2:5]
	v_mfma_f32_16x16x32_bf16 v[62:65], v[186:189], v[202:205], v[62:65]
	v_mfma_f32_16x16x32_bf16 v[50:53], v[194:197], v[202:205], v[50:53]
	v_mfma_f32_16x16x32_bf16 v[46:49], v[186:189], v[210:213], v[46:49]
	v_mfma_f32_16x16x32_bf16 v[34:37], v[194:197], v[210:213], v[34:37]
	v_mfma_f32_16x16x32_bf16 v[30:33], v[186:189], v[220:223], v[30:33]
	v_mfma_f32_16x16x32_bf16 v[18:21], v[194:197], v[220:223], v[18:21]
	v_mfma_f32_16x16x32_bf16 v[14:17], v[186:189], v[228:231], v[14:17]
	v_mfma_f32_16x16x32_bf16 v[2:5], v[194:197], v[228:231], v[2:5]
	s_barrier
	s_add_i32 s33, 0, 0x18000
	v_add_u32_e32 v136, s33, v167
	s_add_i32 s8, 0, 0x1c000
	ds_read_b128 v[144:147], v136
	ds_read_b128 v[148:151], v136 offset:1024
	ds_read_b128 v[174:177], v136 offset:2048
	ds_read_b128 v[178:181], v136 offset:3072
	v_add_u32_e32 v136, s8, v167
	ds_read_b128 v[182:185], v136
	ds_read_b128 v[186:189], v136 offset:1024
	ds_read_b128 v[190:193], v136 offset:2048
	ds_read_b128 v[194:197], v136 offset:3072
	s_add_u32 s26, s82, 0x80000
	s_addc_u32 s27, s83, 0
	s_mov_b32 m0, s89
	v_lshl_add_u64 v[236:237], s[26:27], 0, v[130:131]
	ds_read_b128 v[198:201], v172 offset:32768
	ds_read_b128 v[202:205], v172 offset:33792
	ds_read_b128 v[206:209], v172 offset:34816
	ds_read_b128 v[210:213], v172 offset:35840
	ds_read_b128 v[214:217], v172 offset:36864
	ds_read_b128 v[220:223], v172 offset:37888
	ds_read_b128 v[224:227], v172 offset:38912
	ds_read_b128 v[228:231], v172 offset:39936
	global_load_lds_dwordx4 v[236:237], off
	v_lshl_add_u64 v[236:237], s[26:27], 0, v[132:133]
	s_mov_b32 m0, s90
	s_nop 0
	global_load_lds_dwordx4 v[236:237], off
	s_waitcnt vmcnt(8)
	s_waitcnt lgkmcnt(0)
	s_barrier
	s_waitcnt lgkmcnt(0)
	v_mfma_f32_16x16x32_bf16 v[122:125], v[144:147], v[198:201], v[122:125]
	v_mfma_f32_16x16x32_bf16 v[118:121], v[174:177], v[198:201], v[118:121]
	v_lshl_add_u64 v[242:243], v[240:241], 0, s[20:21]
	v_mfma_f32_16x16x32_bf16 v[106:109], v[144:147], v[206:209], v[106:109]
	v_mfma_f32_16x16x32_bf16 v[102:105], v[174:177], v[206:209], v[102:105]
	v_lshl_add_u64 v[244:245], v[240:241], 0, s[22:23]
	v_mfma_f32_16x16x32_bf16 v[90:93], v[144:147], v[214:217], v[90:93]
	v_mfma_f32_16x16x32_bf16 v[86:89], v[174:177], v[214:217], v[86:89]
	v_lshl_add_u64 v[248:249], v[240:241], 0, s[40:41]
	v_mfma_f32_16x16x32_bf16 v[74:77], v[144:147], v[224:227], v[74:77]
	v_mfma_f32_16x16x32_bf16 v[70:73], v[174:177], v[224:227], v[70:73]
	v_lshl_add_u64 v[240:241], v[240:241], 0, s[44:45]
	v_mfma_f32_16x16x32_bf16 v[122:125], v[148:151], v[202:205], v[122:125]
	v_mfma_f32_16x16x32_bf16 v[118:121], v[178:181], v[202:205], v[118:121]
	v_lshl_add_u64 v[250:251], v[250:251], 0, s[24:25]
	v_mfma_f32_16x16x32_bf16 v[106:109], v[148:151], v[210:213], v[106:109]
	v_mfma_f32_16x16x32_bf16 v[102:105], v[178:181], v[210:213], v[102:105]
	v_lshl_add_u64 v[246:247], v[246:247], 0, s[24:25]
	v_mfma_f32_16x16x32_bf16 v[90:93], v[148:151], v[220:223], v[90:93]
	v_mfma_f32_16x16x32_bf16 v[86:89], v[178:181], v[220:223], v[86:89]
	v_mfma_f32_16x16x32_bf16 v[74:77], v[148:151], v[228:231], v[74:77]
	v_mfma_f32_16x16x32_bf16 v[70:73], v[178:181], v[228:231], v[70:73]
	v_mfma_f32_16x16x32_bf16 v[126:129], v[182:185], v[198:201], v[126:129]
	v_mfma_f32_16x16x32_bf16 v[114:117], v[190:193], v[198:201], v[114:117]
	v_mfma_f32_16x16x32_bf16 v[110:113], v[182:185], v[206:209], v[110:113]
	v_mfma_f32_16x16x32_bf16 v[98:101], v[190:193], v[206:209], v[98:101]
	v_mfma_f32_16x16x32_bf16 v[94:97], v[182:185], v[214:217], v[94:97]
	v_mfma_f32_16x16x32_bf16 v[82:85], v[190:193], v[214:217], v[82:85]
	v_mfma_f32_16x16x32_bf16 v[78:81], v[182:185], v[224:227], v[78:81]
	v_mfma_f32_16x16x32_bf16 v[66:69], v[190:193], v[224:227], v[66:69]
	v_mfma_f32_16x16x32_bf16 v[126:129], v[186:189], v[202:205], v[126:129]
	v_mfma_f32_16x16x32_bf16 v[114:117], v[194:197], v[202:205], v[114:117]
	v_mfma_f32_16x16x32_bf16 v[110:113], v[186:189], v[210:213], v[110:113]
	v_mfma_f32_16x16x32_bf16 v[98:101], v[194:197], v[210:213], v[98:101]
	v_mfma_f32_16x16x32_bf16 v[94:97], v[186:189], v[220:223], v[94:97]
	v_mfma_f32_16x16x32_bf16 v[82:85], v[194:197], v[220:223], v[82:85]
	v_mfma_f32_16x16x32_bf16 v[78:81], v[186:189], v[228:231], v[78:81]
	v_mfma_f32_16x16x32_bf16 v[66:69], v[194:197], v[228:231], v[66:69]
	s_barrier
	s_add_i32 s9, s33, s86
	s_mov_b32 m0, s9
	ds_read_b128 v[198:201], v172 offset:49152
	ds_read_b128 v[202:205], v172 offset:50176
	ds_read_b128 v[206:209], v172 offset:51200
	ds_read_b128 v[210:213], v172 offset:52224
	ds_read_b128 v[214:217], v172 offset:53248
	ds_read_b128 v[220:223], v172 offset:54272
	ds_read_b128 v[224:227], v172 offset:55296
	ds_read_b128 v[228:231], v172 offset:56320
	global_load_lds_dwordx4 v[242:243], off
	s_add_i32 m0, s9, 0x2000
	s_add_i32 s8, s8, s86
	global_load_lds_dwordx4 v[244:245], off
	s_mov_b32 m0, s8
	s_nop 0
	global_load_lds_dwordx4 v[248:249], off
	s_add_i32 m0, s8, 0x2000
	s_nop 0
	global_load_lds_dwordx4 v[240:241], off
	s_mov_b32 m0, s91
	s_nop 0
	global_load_lds_dwordx4 v[250:251], off
	s_mov_b32 m0, s92
	s_nop 0
	global_load_lds_dwordx4 v[246:247], off
	s_waitcnt vmcnt(8)
	s_waitcnt lgkmcnt(0)
	s_barrier
	s_waitcnt lgkmcnt(0)
	v_mfma_f32_16x16x32_bf16 v[58:61], v[144:147], v[198:201], v[58:61]
	v_mfma_f32_16x16x32_bf16 v[54:57], v[174:177], v[198:201], v[54:57]
	v_mfma_f32_16x16x32_bf16 v[42:45], v[144:147], v[206:209], v[42:45]
	v_mfma_f32_16x16x32_bf16 v[38:41], v[174:177], v[206:209], v[38:41]
	v_mfma_f32_16x16x32_bf16 v[26:29], v[144:147], v[214:217], v[26:29]
	v_mfma_f32_16x16x32_bf16 v[22:25], v[174:177], v[214:217], v[22:25]
	v_mfma_f32_16x16x32_bf16 v[10:13], v[144:147], v[224:227], v[10:13]
	v_mfma_f32_16x16x32_bf16 v[6:9], v[174:177], v[224:227], v[6:9]
	v_mfma_f32_16x16x32_bf16 v[58:61], v[148:151], v[202:205], v[58:61]
	v_mfma_f32_16x16x32_bf16 v[54:57], v[178:181], v[202:205], v[54:57]
	v_mfma_f32_16x16x32_bf16 v[42:45], v[148:151], v[210:213], v[42:45]
	v_mfma_f32_16x16x32_bf16 v[38:41], v[178:181], v[210:213], v[38:41]
	v_mfma_f32_16x16x32_bf16 v[26:29], v[148:151], v[220:223], v[26:29]
	v_mfma_f32_16x16x32_bf16 v[22:25], v[178:181], v[220:223], v[22:25]
	v_mfma_f32_16x16x32_bf16 v[10:13], v[148:151], v[228:231], v[10:13]
	v_mfma_f32_16x16x32_bf16 v[6:9], v[178:181], v[228:231], v[6:9]
	v_mfma_f32_16x16x32_bf16 v[62:65], v[182:185], v[198:201], v[62:65]
	v_mfma_f32_16x16x32_bf16 v[50:53], v[190:193], v[198:201], v[50:53]
	v_mfma_f32_16x16x32_bf16 v[46:49], v[182:185], v[206:209], v[46:49]
	v_mfma_f32_16x16x32_bf16 v[34:37], v[190:193], v[206:209], v[34:37]
	v_mfma_f32_16x16x32_bf16 v[30:33], v[182:185], v[214:217], v[30:33]
	v_mfma_f32_16x16x32_bf16 v[18:21], v[190:193], v[214:217], v[18:21]
	v_mfma_f32_16x16x32_bf16 v[14:17], v[182:185], v[224:227], v[14:17]
	v_mfma_f32_16x16x32_bf16 v[2:5], v[190:193], v[224:227], v[2:5]
	v_mfma_f32_16x16x32_bf16 v[62:65], v[186:189], v[202:205], v[62:65]
	v_mfma_f32_16x16x32_bf16 v[50:53], v[194:197], v[202:205], v[50:53]
	v_mfma_f32_16x16x32_bf16 v[46:49], v[186:189], v[210:213], v[46:49]
	v_mfma_f32_16x16x32_bf16 v[34:37], v[194:197], v[210:213], v[34:37]
	v_mfma_f32_16x16x32_bf16 v[30:33], v[186:189], v[220:223], v[30:33]
	v_mfma_f32_16x16x32_bf16 v[18:21], v[194:197], v[220:223], v[18:21]
	v_mfma_f32_16x16x32_bf16 v[14:17], v[186:189], v[228:231], v[14:17]
	v_mfma_f32_16x16x32_bf16 v[2:5], v[194:197], v[228:231], v[2:5]
	s_barrier
	s_add_i32 vcc_hi, vcc_hi, 2
	s_add_u32 s97, s97, 0x10000
	s_addc_u32 vcc_lo, vcc_lo, 0
	s_add_u32 s80, s80, 0x100
	s_addc_u32 s81, s81, 0
	s_cmp_gt_u32 vcc_hi, 29
	s_cbranch_scc0 .LBB0_261
	s_and_b64 vcc, exec, s[50:51]
	s_cbranch_vccz .LBB0_264
	s_barrier

.LBB0_285:
	ds_read_b128 v[26:29], v1
	ds_read_b128 v[30:33], v1 offset:1024
	ds_read_b128 v[18:21], v1 offset:2048
	ds_read_b128 v[22:25], v1 offset:3072
	ds_read_b128 v[10:13], v185
	ds_read_b128 v[14:17], v185 offset:1024
	ds_read_b128 v[2:5], v185 offset:2048
	ds_read_b128 v[6:9], v185 offset:3072
	s_add_u32 s26, s70, 0xfffc0080
	s_addc_u32 s27, s71, -1
	s_cmp_eq_u32 s94, 12
	s_cselect_b32 s73, s51, s27
	s_cselect_b32 s72, s90, s26
	s_cselect_b32 s75, s45, s93
	s_cselect_b32 s74, s91, s92
	v_lshl_add_u64 v[176:177], s[70:71], 0, v[168:169]
	s_add_i32 m0, s33, 0xc000
	ds_read_b128 v[190:193], v186
	ds_read_b128 v[194:197], v186 offset:1024
	ds_read_b128 v[198:201], v186 offset:2048
	ds_read_b128 v[202:205], v186 offset:3072
	ds_read_b128 v[206:209], v186 offset:4096
	ds_read_b128 v[210:213], v186 offset:5120
	ds_read_b128 v[220:223], v186 offset:6144
	ds_read_b128 v[224:227], v186 offset:7168
	global_load_lds_dwordx4 v[176:177], off
	v_lshl_add_u64 v[176:177], s[70:71], 0, v[170:171]
	s_add_i32 m0, s33, 0xe000
	s_nop 0
	global_load_lds_dwordx4 v[176:177], off
	s_waitcnt vmcnt(8)
	s_waitcnt lgkmcnt(0)
	s_barrier
	s_waitcnt lgkmcnt(0)
	v_mfma_scale_f32_16x16x128_f8f6f4 v[158:161], v[26:33], v[190:197], v[158:161], v187, v188 op_sel_hi:[0,0,0]
	v_mfma_scale_f32_16x16x128_f8f6f4 v[154:157], v[18:25], v[190:197], v[154:157], v187, v188 op_sel_hi:[0,0,0]
	v_lshl_add_u64 v[240:241], s[74:75], 0, v[162:163]
	v_mfma_scale_f32_16x16x128_f8f6f4 v[150:153], v[26:33], v[198:205], v[150:153], v187, v188 op_sel_hi:[0,0,0]
	v_mfma_scale_f32_16x16x128_f8f6f4 v[142:145], v[18:25], v[198:205], v[142:145], v187, v188 op_sel_hi:[0,0,0]
	v_lshl_add_u64 v[242:243], v[240:241], 0, s[8:9]
	v_mfma_scale_f32_16x16x128_f8f6f4 v[134:137], v[26:33], v[206:213], v[134:137], v187, v188 op_sel_hi:[0,0,0]
	v_mfma_scale_f32_16x16x128_f8f6f4 v[126:129], v[18:25], v[206:213], v[126:129], v187, v188 op_sel_hi:[0,0,0]
	v_lshl_add_u64 v[244:245], v[240:241], 0, s[10:11]
	v_mfma_scale_f32_16x16x128_f8f6f4 v[118:121], v[26:33], v[220:227], v[118:121], v187, v188 op_sel_hi:[0,0,0]
	v_mfma_scale_f32_16x16x128_f8f6f4 v[110:113], v[18:25], v[220:227], v[110:113], v187, v188 op_sel_hi:[0,0,0]
	v_lshl_add_u64 v[246:247], s[72:73], 0, v[166:167]
	v_mfma_scale_f32_16x16x128_f8f6f4 v[146:149], v[10:17], v[190:197], v[146:149], v187, v188 op_sel_hi:[0,0,0]
	v_mfma_scale_f32_16x16x128_f8f6f4 v[138:141], v[2:9], v[190:197], v[138:141], v187, v188 op_sel_hi:[0,0,0]
	v_lshl_add_u64 v[248:249], v[240:241], 0, s[12:13]
	v_mfma_scale_f32_16x16x128_f8f6f4 v[130:133], v[10:17], v[198:205], v[130:133], v187, v188 op_sel_hi:[0,0,0]
	v_mfma_scale_f32_16x16x128_f8f6f4 v[122:125], v[2:9], v[198:205], v[122:125], v187, v188 op_sel_hi:[0,0,0]
	v_lshl_add_u64 v[250:251], s[72:73], 0, v[164:165]
	v_mfma_scale_f32_16x16x128_f8f6f4 v[114:117], v[10:17], v[206:213], v[114:117], v187, v188 op_sel_hi:[0,0,0]
	v_mfma_scale_f32_16x16x128_f8f6f4 v[106:109], v[2:9], v[206:213], v[106:109], v187, v188 op_sel_hi:[0,0,0]
	v_mfma_scale_f32_16x16x128_f8f6f4 v[102:105], v[10:17], v[220:227], v[102:105], v187, v188 op_sel_hi:[0,0,0]
	v_mfma_scale_f32_16x16x128_f8f6f4 v[98:101], v[2:9], v[220:227], v[98:101], v187, v188 op_sel_hi:[0,0,0]
	s_barrier
	s_add_i32 s26, s88, s80
	s_mov_b32 m0, s26
	ds_read_b128 v[190:193], v186 offset:16384
	ds_read_b128 v[194:197], v186 offset:17408
	ds_read_b128 v[198:201], v186 offset:18432
	ds_read_b128 v[202:205], v186 offset:19456
	ds_read_b128 v[206:209], v186 offset:20480
	ds_read_b128 v[210:213], v186 offset:21504
	ds_read_b128 v[220:223], v186 offset:22528
	ds_read_b128 v[224:227], v186 offset:23552
	global_load_lds_dwordx4 v[240:241], off
	s_add_i32 m0, s26, 0x2000
	s_add_i32 s26, s89, s80
	global_load_lds_dwordx4 v[242:243], off
	s_mov_b32 m0, s26
	s_nop 0
	global_load_lds_dwordx4 v[244:245], off
	s_add_i32 m0, s26, 0x2000
	s_nop 0
	global_load_lds_dwordx4 v[248:249], off
	s_mov_b32 m0, s33
	s_nop 0
	global_load_lds_dwordx4 v[250:251], off
	s_mov_b32 m0, s69
	s_nop 0
	global_load_lds_dwordx4 v[246:247], off
	s_waitcnt vmcnt(8)
	s_waitcnt lgkmcnt(0)
	s_barrier
	s_waitcnt lgkmcnt(0)
	v_mfma_scale_f32_16x16x128_f8f6f4 v[94:97], v[26:33], v[190:197], v[94:97], v187, v188 op_sel_hi:[0,0,0]
	v_mfma_scale_f32_16x16x128_f8f6f4 v[90:93], v[18:25], v[190:197], v[90:93], v187, v188 op_sel_hi:[0,0,0]
	v_mfma_scale_f32_16x16x128_f8f6f4 v[86:89], v[26:33], v[198:205], v[86:89], v187, v188 op_sel_hi:[0,0,0]
	v_mfma_scale_f32_16x16x128_f8f6f4 v[78:81], v[18:25], v[198:205], v[78:81], v187, v188 op_sel_hi:[0,0,0]
	v_mfma_scale_f32_16x16x128_f8f6f4 v[70:73], v[26:33], v[206:213], v[70:73], v187, v188 op_sel_hi:[0,0,0]
	v_mfma_scale_f32_16x16x128_f8f6f4 v[62:65], v[18:25], v[206:213], v[62:65], v187, v188 op_sel_hi:[0,0,0]
	v_mfma_scale_f32_16x16x128_f8f6f4 v[54:57], v[26:33], v[220:227], v[54:57], v187, v188 op_sel_hi:[0,0,0]
	v_mfma_scale_f32_16x16x128_f8f6f4 v[46:49], v[18:25], v[220:227], v[46:49], v187, v188 op_sel_hi:[0,0,0]
	v_mfma_scale_f32_16x16x128_f8f6f4 v[82:85], v[10:17], v[190:197], v[82:85], v187, v188 op_sel_hi:[0,0,0]
	v_mfma_scale_f32_16x16x128_f8f6f4 v[74:77], v[2:9], v[190:197], v[74:77], v187, v188 op_sel_hi:[0,0,0]
	v_mfma_scale_f32_16x16x128_f8f6f4 v[66:69], v[10:17], v[198:205], v[66:69], v187, v188 op_sel_hi:[0,0,0]
	v_mfma_scale_f32_16x16x128_f8f6f4 v[58:61], v[2:9], v[198:205], v[58:61], v187, v188 op_sel_hi:[0,0,0]
	v_mfma_scale_f32_16x16x128_f8f6f4 v[50:53], v[10:17], v[206:213], v[50:53], v187, v188 op_sel_hi:[0,0,0]
	v_mfma_scale_f32_16x16x128_f8f6f4 v[42:45], v[2:9], v[206:213], v[42:45], v187, v188 op_sel_hi:[0,0,0]
	v_mfma_scale_f32_16x16x128_f8f6f4 v[38:41], v[10:17], v[220:227], v[38:41], v187, v188 op_sel_hi:[0,0,0]
	v_mfma_scale_f32_16x16x128_f8f6f4 v[34:37], v[2:9], v[220:227], v[34:37], v187, v188 op_sel_hi:[0,0,0]
	s_barrier
	s_add_i32 s74, 0, 0x18000
	s_add_i32 s75, 0, 0x1c000
	v_add_u32_e32 v14, s74, v183
	v_add_u32_e32 v30, s75, v183
	ds_read_b128 v[2:5], v14
	ds_read_b128 v[6:9], v14 offset:1024
	ds_read_b128 v[10:13], v14 offset:2048
	ds_read_b128 v[14:17], v14 offset:3072
	ds_read_b128 v[18:21], v30
	ds_read_b128 v[22:25], v30 offset:1024
	ds_read_b128 v[26:29], v30 offset:2048
	ds_read_b128 v[30:33], v30 offset:3072
	s_add_u32 s26, s72, 0x40000
	s_addc_u32 s27, s73, 0
	s_mov_b32 m0, s83
	v_lshl_add_u64 v[214:215], s[26:27], 0, v[164:165]
	ds_read_b128 v[190:193], v186 offset:32768
	ds_read_b128 v[194:197], v186 offset:33792
	ds_read_b128 v[198:201], v186 offset:34816
	ds_read_b128 v[202:205], v186 offset:35840
	ds_read_b128 v[206:209], v186 offset:36864
	ds_read_b128 v[210:213], v186 offset:37888
	ds_read_b128 v[220:223], v186 offset:38912
	ds_read_b128 v[224:227], v186 offset:39936
	global_load_lds_dwordx4 v[214:215], off
	v_lshl_add_u64 v[214:215], s[26:27], 0, v[166:167]
	s_mov_b32 m0, s84
	s_nop 0
	global_load_lds_dwordx4 v[214:215], off
	s_waitcnt vmcnt(8)
	s_waitcnt lgkmcnt(0)
	s_barrier
	s_waitcnt lgkmcnt(0)
	v_mfma_scale_f32_16x16x128_f8f6f4 v[158:161], v[2:9], v[190:197], v[158:161], v187, v188 op_sel_hi:[0,0,0]
	v_mfma_scale_f32_16x16x128_f8f6f4 v[154:157], v[10:17], v[190:197], v[154:157], v187, v188 op_sel_hi:[0,0,0]
	v_lshl_add_u64 v[242:243], v[240:241], 0, s[16:17]
	v_mfma_scale_f32_16x16x128_f8f6f4 v[150:153], v[2:9], v[198:205], v[150:153], v187, v188 op_sel_hi:[0,0,0]
	v_mfma_scale_f32_16x16x128_f8f6f4 v[142:145], v[10:17], v[198:205], v[142:145], v187, v188 op_sel_hi:[0,0,0]
	v_lshl_add_u64 v[244:245], v[240:241], 0, s[18:19]
	v_mfma_scale_f32_16x16x128_f8f6f4 v[134:137], v[2:9], v[206:213], v[134:137], v187, v188 op_sel_hi:[0,0,0]
	v_mfma_scale_f32_16x16x128_f8f6f4 v[126:129], v[10:17], v[206:213], v[126:129], v187, v188 op_sel_hi:[0,0,0]
	v_lshl_add_u64 v[248:249], v[240:241], 0, s[22:23]
	v_mfma_scale_f32_16x16x128_f8f6f4 v[118:121], v[2:9], v[220:227], v[118:121], v187, v188 op_sel_hi:[0,0,0]
	v_mfma_scale_f32_16x16x128_f8f6f4 v[110:113], v[10:17], v[220:227], v[110:113], v187, v188 op_sel_hi:[0,0,0]
	v_lshl_add_u64 v[240:241], v[240:241], 0, s[24:25]
	v_mfma_scale_f32_16x16x128_f8f6f4 v[146:149], v[18:25], v[190:197], v[146:149], v187, v188 op_sel_hi:[0,0,0]
	v_mfma_scale_f32_16x16x128_f8f6f4 v[138:141], v[26:33], v[190:197], v[138:141], v187, v188 op_sel_hi:[0,0,0]
	v_lshl_add_u64 v[250:251], v[250:251], 0, s[20:21]
	v_mfma_scale_f32_16x16x128_f8f6f4 v[130:133], v[18:25], v[198:205], v[130:133], v187, v188 op_sel_hi:[0,0,0]
	v_mfma_scale_f32_16x16x128_f8f6f4 v[122:125], v[26:33], v[198:205], v[122:125], v187, v188 op_sel_hi:[0,0,0]
	v_lshl_add_u64 v[246:247], v[246:247], 0, s[20:21]
	v_mfma_scale_f32_16x16x128_f8f6f4 v[114:117], v[18:25], v[206:213], v[114:117], v187, v188 op_sel_hi:[0,0,0]
	v_mfma_scale_f32_16x16x128_f8f6f4 v[106:109], v[26:33], v[206:213], v[106:109], v187, v188 op_sel_hi:[0,0,0]
	v_mfma_scale_f32_16x16x128_f8f6f4 v[102:105], v[18:25], v[220:227], v[102:105], v187, v188 op_sel_hi:[0,0,0]
	v_mfma_scale_f32_16x16x128_f8f6f4 v[98:101], v[26:33], v[220:227], v[98:101], v187, v188 op_sel_hi:[0,0,0]
	s_barrier
	s_add_i32 s26, s74, s80
	s_mov_b32 m0, s26
	ds_read_b128 v[190:193], v186 offset:49152
	ds_read_b128 v[194:197], v186 offset:50176
	ds_read_b128 v[198:201], v186 offset:51200
	ds_read_b128 v[202:205], v186 offset:52224
	ds_read_b128 v[206:209], v186 offset:53248
	ds_read_b128 v[210:213], v186 offset:54272
	ds_read_b128 v[220:223], v186 offset:55296
	ds_read_b128 v[224:227], v186 offset:56320
	global_load_lds_dwordx4 v[242:243], off
	s_add_i32 m0, s26, 0x2000
	s_add_i32 s26, s75, s80
	global_load_lds_dwordx4 v[244:245], off
	s_mov_b32 m0, s26
	s_nop 0
	global_load_lds_dwordx4 v[248:249], off
	s_add_i32 m0, s26, 0x2000
	s_nop 0
	global_load_lds_dwordx4 v[240:241], off
	s_mov_b32 m0, s86
	s_nop 0
	global_load_lds_dwordx4 v[250:251], off
	s_mov_b32 m0, s87
	s_nop 0
	global_load_lds_dwordx4 v[246:247], off
	s_waitcnt vmcnt(8)
	s_waitcnt lgkmcnt(0)
	s_barrier
	s_waitcnt lgkmcnt(0)
	v_mfma_scale_f32_16x16x128_f8f6f4 v[94:97], v[2:9], v[190:197], v[94:97], v187, v188 op_sel_hi:[0,0,0]
	v_mfma_scale_f32_16x16x128_f8f6f4 v[90:93], v[10:17], v[190:197], v[90:93], v187, v188 op_sel_hi:[0,0,0]
	v_mfma_scale_f32_16x16x128_f8f6f4 v[86:89], v[2:9], v[198:205], v[86:89], v187, v188 op_sel_hi:[0,0,0]
	v_mfma_scale_f32_16x16x128_f8f6f4 v[78:81], v[10:17], v[198:205], v[78:81], v187, v188 op_sel_hi:[0,0,0]
	v_mfma_scale_f32_16x16x128_f8f6f4 v[70:73], v[2:9], v[206:213], v[70:73], v187, v188 op_sel_hi:[0,0,0]
	v_mfma_scale_f32_16x16x128_f8f6f4 v[62:65], v[10:17], v[206:213], v[62:65], v187, v188 op_sel_hi:[0,0,0]
	v_mfma_scale_f32_16x16x128_f8f6f4 v[54:57], v[2:9], v[220:227], v[54:57], v187, v188 op_sel_hi:[0,0,0]
	v_mfma_scale_f32_16x16x128_f8f6f4 v[46:49], v[10:17], v[220:227], v[46:49], v187, v188 op_sel_hi:[0,0,0]
	v_mfma_scale_f32_16x16x128_f8f6f4 v[82:85], v[18:25], v[190:197], v[82:85], v187, v188 op_sel_hi:[0,0,0]
	v_mfma_scale_f32_16x16x128_f8f6f4 v[74:77], v[26:33], v[190:197], v[74:77], v187, v188 op_sel_hi:[0,0,0]
	v_mfma_scale_f32_16x16x128_f8f6f4 v[66:69], v[18:25], v[198:205], v[66:69], v187, v188 op_sel_hi:[0,0,0]
	v_mfma_scale_f32_16x16x128_f8f6f4 v[58:61], v[26:33], v[198:205], v[58:61], v187, v188 op_sel_hi:[0,0,0]
	v_mfma_scale_f32_16x16x128_f8f6f4 v[50:53], v[18:25], v[206:213], v[50:53], v187, v188 op_sel_hi:[0,0,0]
	v_mfma_scale_f32_16x16x128_f8f6f4 v[42:45], v[26:33], v[206:213], v[42:45], v187, v188 op_sel_hi:[0,0,0]
	v_mfma_scale_f32_16x16x128_f8f6f4 v[38:41], v[18:25], v[220:227], v[38:41], v187, v188 op_sel_hi:[0,0,0]
	v_mfma_scale_f32_16x16x128_f8f6f4 v[34:37], v[26:33], v[220:227], v[34:37], v187, v188 op_sel_hi:[0,0,0]
	s_barrier
	s_add_i32 s94, s94, 2
	s_add_u32 s92, s92, 0x10000
	s_addc_u32 s93, s93, 0
	s_add_u32 s70, s70, 0x100
	s_addc_u32 s71, s71, 0
	s_cmp_gt_u32 s94, 13
	s_cbranch_scc0 .LBB0_285
	s_and_b64 vcc, exec, s[40:41]
	s_cbranch_vccz .LBB0_288
	s_barrier

.LBB0_660:
	ds_read_b128 v[130:133], v222
	ds_read_b128 v[134:137], v222 offset:1024
	ds_read_b128 v[138:141], v222 offset:2048
	ds_read_b128 v[142:145], v222 offset:3072
	ds_read_b128 v[146:149], v223
	ds_read_b128 v[150:153], v223 offset:1024
	ds_read_b128 v[154:157], v223 offset:2048
	ds_read_b128 v[158:161], v223 offset:3072
	s_add_u32 s26, s58, 0xfff80080
	s_addc_u32 s27, s59, -1
	s_cmp_eq_u32 s80, 28
	s_cselect_b32 s61, s45, s27
	s_cselect_b32 s60, s72, s26
	s_cselect_b32 s27, s41, s75
	s_cselect_b32 s26, s73, s74
	v_lshl_add_u64 v[208:209], s[58:59], 0, v[200:201]
	s_add_i32 m0, s57, 0xc000
	ds_read_b128 v[162:165], v224
	ds_read_b128 v[166:169], v224 offset:1024
	ds_read_b128 v[170:173], v224 offset:2048
	ds_read_b128 v[174:177], v224 offset:3072
	ds_read_b128 v[178:181], v224 offset:4096
	ds_read_b128 v[182:185], v224 offset:5120
	ds_read_b128 v[186:189], v224 offset:6144
	ds_read_b128 v[190:193], v224 offset:7168
	global_load_lds_dwordx4 v[208:209], off
	v_lshl_add_u64 v[208:209], s[58:59], 0, v[202:203]
	s_add_i32 m0, s57, 0xe000
	s_nop 0
	global_load_lds_dwordx4 v[208:209], off
	s_waitcnt vmcnt(8)
	s_waitcnt lgkmcnt(0)
	s_barrier
	s_waitcnt lgkmcnt(0)
	v_mfma_f32_16x16x32_bf16 v[126:129], v[130:133], v[162:165], v[126:129]
	v_mfma_f32_16x16x32_bf16 v[122:125], v[138:141], v[162:165], v[122:125]
	v_lshl_add_u64 v[240:241], s[26:27], 0, v[194:195]
	v_mfma_f32_16x16x32_bf16 v[118:121], v[130:133], v[170:173], v[118:121]
	v_mfma_f32_16x16x32_bf16 v[114:117], v[138:141], v[170:173], v[114:117]
	v_lshl_add_u64 v[242:243], v[240:241], 0, s[6:7]
	v_mfma_f32_16x16x32_bf16 v[110:113], v[130:133], v[178:181], v[110:113]
	v_mfma_f32_16x16x32_bf16 v[102:105], v[138:141], v[178:181], v[102:105]
	v_lshl_add_u64 v[244:245], v[240:241], 0, s[8:9]
	v_mfma_f32_16x16x32_bf16 v[94:97], v[130:133], v[186:189], v[94:97]
	v_mfma_f32_16x16x32_bf16 v[74:77], v[138:141], v[186:189], v[74:77]
	v_lshl_add_u64 v[246:247], s[60:61], 0, v[198:199]
	v_mfma_f32_16x16x32_bf16 v[126:129], v[134:137], v[166:169], v[126:129]
	v_mfma_f32_16x16x32_bf16 v[122:125], v[142:145], v[166:169], v[122:125]
	v_lshl_add_u64 v[248:249], v[240:241], 0, s[10:11]
	v_mfma_f32_16x16x32_bf16 v[118:121], v[134:137], v[174:177], v[118:121]
	v_mfma_f32_16x16x32_bf16 v[114:117], v[142:145], v[174:177], v[114:117]
	v_lshl_add_u64 v[250:251], s[60:61], 0, v[196:197]
	v_mfma_f32_16x16x32_bf16 v[110:113], v[134:137], v[182:185], v[110:113]
	v_mfma_f32_16x16x32_bf16 v[102:105], v[142:145], v[182:185], v[102:105]
	v_mfma_f32_16x16x32_bf16 v[94:97], v[134:137], v[190:193], v[94:97]
	v_mfma_f32_16x16x32_bf16 v[74:77], v[142:145], v[190:193], v[74:77]
	v_mfma_f32_16x16x32_bf16 v[106:109], v[146:149], v[162:165], v[106:109]
	v_mfma_f32_16x16x32_bf16 v[98:101], v[154:157], v[162:165], v[98:101]
	v_mfma_f32_16x16x32_bf16 v[90:93], v[146:149], v[170:173], v[90:93]
	v_mfma_f32_16x16x32_bf16 v[86:89], v[154:157], v[170:173], v[86:89]
	v_mfma_f32_16x16x32_bf16 v[82:85], v[146:149], v[178:181], v[82:85]
	v_mfma_f32_16x16x32_bf16 v[78:81], v[154:157], v[178:181], v[78:81]
	v_mfma_f32_16x16x32_bf16 v[70:73], v[146:149], v[186:189], v[70:73]
	v_mfma_f32_16x16x32_bf16 v[66:69], v[154:157], v[186:189], v[66:69]
	v_mfma_f32_16x16x32_bf16 v[106:109], v[150:153], v[166:169], v[106:109]
	v_mfma_f32_16x16x32_bf16 v[98:101], v[158:161], v[166:169], v[98:101]
	v_mfma_f32_16x16x32_bf16 v[90:93], v[150:153], v[174:177], v[90:93]
	v_mfma_f32_16x16x32_bf16 v[86:89], v[158:161], v[174:177], v[86:89]
	v_mfma_f32_16x16x32_bf16 v[82:85], v[150:153], v[182:185], v[82:85]
	v_mfma_f32_16x16x32_bf16 v[78:81], v[158:161], v[182:185], v[78:81]
	v_mfma_f32_16x16x32_bf16 v[70:73], v[150:153], v[190:193], v[70:73]
	v_mfma_f32_16x16x32_bf16 v[66:69], v[158:161], v[190:193], v[66:69]
	s_barrier
	s_add_i32 s26, s70, s35
	s_mov_b32 m0, s26
	ds_read_b128 v[162:165], v224 offset:16384
	ds_read_b128 v[166:169], v224 offset:17408
	ds_read_b128 v[170:173], v224 offset:18432
	ds_read_b128 v[174:177], v224 offset:19456
	ds_read_b128 v[178:181], v224 offset:20480
	ds_read_b128 v[182:185], v224 offset:21504
	ds_read_b128 v[186:189], v224 offset:22528
	ds_read_b128 v[190:193], v224 offset:23552
	global_load_lds_dwordx4 v[240:241], off
	s_add_i32 m0, s26, 0x2000
	s_add_i32 s26, s71, s35
	global_load_lds_dwordx4 v[242:243], off
	s_mov_b32 m0, s26
	s_nop 0
	global_load_lds_dwordx4 v[244:245], off
	s_add_i32 m0, s26, 0x2000
	s_nop 0
	global_load_lds_dwordx4 v[248:249], off
	s_mov_b32 m0, s57
	s_nop 0
	global_load_lds_dwordx4 v[250:251], off
	s_mov_b32 m0, s63
	s_nop 0
	global_load_lds_dwordx4 v[246:247], off
	s_waitcnt vmcnt(8)
	s_waitcnt lgkmcnt(0)
	s_barrier
	s_waitcnt lgkmcnt(0)
	v_mfma_f32_16x16x32_bf16 v[62:65], v[130:133], v[162:165], v[62:65]
	v_mfma_f32_16x16x32_bf16 v[58:61], v[138:141], v[162:165], v[58:61]
	v_mfma_f32_16x16x32_bf16 v[54:57], v[130:133], v[170:173], v[54:57]
	v_mfma_f32_16x16x32_bf16 v[50:53], v[138:141], v[170:173], v[50:53]
	v_mfma_f32_16x16x32_bf16 v[46:49], v[130:133], v[178:181], v[46:49]
	v_mfma_f32_16x16x32_bf16 v[38:41], v[138:141], v[178:181], v[38:41]
	v_mfma_f32_16x16x32_bf16 v[30:33], v[130:133], v[186:189], v[30:33]
	v_mfma_f32_16x16x32_bf16 v[10:13], v[138:141], v[186:189], v[10:13]
	v_mfma_f32_16x16x32_bf16 v[62:65], v[134:137], v[166:169], v[62:65]
	v_mfma_f32_16x16x32_bf16 v[58:61], v[142:145], v[166:169], v[58:61]
	v_mfma_f32_16x16x32_bf16 v[54:57], v[134:137], v[174:177], v[54:57]
	v_mfma_f32_16x16x32_bf16 v[50:53], v[142:145], v[174:177], v[50:53]
	v_mfma_f32_16x16x32_bf16 v[46:49], v[134:137], v[182:185], v[46:49]
	v_mfma_f32_16x16x32_bf16 v[38:41], v[142:145], v[182:185], v[38:41]
	v_mfma_f32_16x16x32_bf16 v[30:33], v[134:137], v[190:193], v[30:33]
	v_mfma_f32_16x16x32_bf16 v[10:13], v[142:145], v[190:193], v[10:13]
	v_mfma_f32_16x16x32_bf16 v[42:45], v[146:149], v[162:165], v[42:45]
	v_mfma_f32_16x16x32_bf16 v[34:37], v[154:157], v[162:165], v[34:37]
	v_mfma_f32_16x16x32_bf16 v[26:29], v[146:149], v[170:173], v[26:29]
	v_mfma_f32_16x16x32_bf16 v[22:25], v[154:157], v[170:173], v[22:25]
	v_mfma_f32_16x16x32_bf16 v[18:21], v[146:149], v[178:181], v[18:21]
	v_mfma_f32_16x16x32_bf16 v[14:17], v[154:157], v[178:181], v[14:17]
	v_mfma_f32_16x16x32_bf16 v[6:9], v[146:149], v[186:189], v[6:9]
	v_mfma_f32_16x16x32_bf16 v[2:5], v[154:157], v[186:189], v[2:5]
	v_mfma_f32_16x16x32_bf16 v[42:45], v[150:153], v[166:169], v[42:45]
	v_mfma_f32_16x16x32_bf16 v[34:37], v[158:161], v[166:169], v[34:37]
	v_mfma_f32_16x16x32_bf16 v[26:29], v[150:153], v[174:177], v[26:29]
	v_mfma_f32_16x16x32_bf16 v[22:25], v[158:161], v[174:177], v[22:25]
	v_mfma_f32_16x16x32_bf16 v[18:21], v[150:153], v[182:185], v[18:21]
	v_mfma_f32_16x16x32_bf16 v[14:17], v[158:161], v[182:185], v[14:17]
	v_mfma_f32_16x16x32_bf16 v[6:9], v[150:153], v[190:193], v[6:9]
	v_mfma_f32_16x16x32_bf16 v[2:5], v[158:161], v[190:193], v[2:5]
	s_barrier
	s_add_i32 s81, 0, 0x18000
	s_add_i32 s82, 0, 0x1c000
	v_add_u32_e32 v142, s81, v220
	v_add_u32_e32 v158, s82, v220
	ds_read_b128 v[130:133], v142
	ds_read_b128 v[134:137], v142 offset:1024
	ds_read_b128 v[138:141], v142 offset:2048
	ds_read_b128 v[142:145], v142 offset:3072
	ds_read_b128 v[146:149], v158
	ds_read_b128 v[150:153], v158 offset:1024
	ds_read_b128 v[154:157], v158 offset:2048
	ds_read_b128 v[158:161], v158 offset:3072
	s_add_u32 s26, s60, 0x80000
	s_addc_u32 s27, s61, 0
	s_mov_b32 m0, s64
	v_lshl_add_u64 v[214:215], s[26:27], 0, v[196:197]
	ds_read_b128 v[162:165], v224 offset:32768
	ds_read_b128 v[166:169], v224 offset:33792
	ds_read_b128 v[170:173], v224 offset:34816
	ds_read_b128 v[174:177], v224 offset:35840
	ds_read_b128 v[178:181], v224 offset:36864
	ds_read_b128 v[182:185], v224 offset:37888
	ds_read_b128 v[186:189], v224 offset:38912
	ds_read_b128 v[190:193], v224 offset:39936
	global_load_lds_dwordx4 v[214:215], off
	v_lshl_add_u64 v[214:215], s[26:27], 0, v[198:199]
	s_mov_b32 m0, s65
	s_nop 0
	global_load_lds_dwordx4 v[214:215], off
	s_waitcnt vmcnt(8)
	s_waitcnt lgkmcnt(0)
	s_barrier
	s_waitcnt lgkmcnt(0)
	v_mfma_f32_16x16x32_bf16 v[126:129], v[130:133], v[162:165], v[126:129]
	v_mfma_f32_16x16x32_bf16 v[122:125], v[138:141], v[162:165], v[122:125]
	v_lshl_add_u64 v[242:243], v[240:241], 0, s[14:15]
	v_mfma_f32_16x16x32_bf16 v[118:121], v[130:133], v[170:173], v[118:121]
	v_mfma_f32_16x16x32_bf16 v[114:117], v[138:141], v[170:173], v[114:117]
	v_lshl_add_u64 v[244:245], v[240:241], 0, s[16:17]
	v_mfma_f32_16x16x32_bf16 v[110:113], v[130:133], v[178:181], v[110:113]
	v_mfma_f32_16x16x32_bf16 v[102:105], v[138:141], v[178:181], v[102:105]
	v_lshl_add_u64 v[248:249], v[240:241], 0, s[20:21]
	v_mfma_f32_16x16x32_bf16 v[94:97], v[130:133], v[186:189], v[94:97]
	v_mfma_f32_16x16x32_bf16 v[74:77], v[138:141], v[186:189], v[74:77]
	v_lshl_add_u64 v[240:241], v[240:241], 0, s[22:23]
	v_mfma_f32_16x16x32_bf16 v[126:129], v[134:137], v[166:169], v[126:129]
	v_mfma_f32_16x16x32_bf16 v[122:125], v[142:145], v[166:169], v[122:125]
	v_lshl_add_u64 v[250:251], v[250:251], 0, s[18:19]
	v_mfma_f32_16x16x32_bf16 v[118:121], v[134:137], v[174:177], v[118:121]
	v_mfma_f32_16x16x32_bf16 v[114:117], v[142:145], v[174:177], v[114:117]
	v_lshl_add_u64 v[246:247], v[246:247], 0, s[18:19]
	v_mfma_f32_16x16x32_bf16 v[110:113], v[134:137], v[182:185], v[110:113]
	v_mfma_f32_16x16x32_bf16 v[102:105], v[142:145], v[182:185], v[102:105]
	v_mfma_f32_16x16x32_bf16 v[94:97], v[134:137], v[190:193], v[94:97]
	v_mfma_f32_16x16x32_bf16 v[74:77], v[142:145], v[190:193], v[74:77]
	v_mfma_f32_16x16x32_bf16 v[106:109], v[146:149], v[162:165], v[106:109]
	v_mfma_f32_16x16x32_bf16 v[98:101], v[154:157], v[162:165], v[98:101]
	v_mfma_f32_16x16x32_bf16 v[90:93], v[146:149], v[170:173], v[90:93]
	v_mfma_f32_16x16x32_bf16 v[86:89], v[154:157], v[170:173], v[86:89]
	v_mfma_f32_16x16x32_bf16 v[82:85], v[146:149], v[178:181], v[82:85]
	v_mfma_f32_16x16x32_bf16 v[78:81], v[154:157], v[178:181], v[78:81]
	v_mfma_f32_16x16x32_bf16 v[70:73], v[146:149], v[186:189], v[70:73]
	v_mfma_f32_16x16x32_bf16 v[66:69], v[154:157], v[186:189], v[66:69]
	v_mfma_f32_16x16x32_bf16 v[106:109], v[150:153], v[166:169], v[106:109]
	v_mfma_f32_16x16x32_bf16 v[98:101], v[158:161], v[166:169], v[98:101]
	v_mfma_f32_16x16x32_bf16 v[90:93], v[150:153], v[174:177], v[90:93]
	v_mfma_f32_16x16x32_bf16 v[86:89], v[158:161], v[174:177], v[86:89]
	v_mfma_f32_16x16x32_bf16 v[82:85], v[150:153], v[182:185], v[82:85]
	v_mfma_f32_16x16x32_bf16 v[78:81], v[158:161], v[182:185], v[78:81]
	v_mfma_f32_16x16x32_bf16 v[70:73], v[150:153], v[190:193], v[70:73]
	v_mfma_f32_16x16x32_bf16 v[66:69], v[158:161], v[190:193], v[66:69]
	s_barrier
	s_add_i32 s26, s81, s35
	s_mov_b32 m0, s26
	ds_read_b128 v[162:165], v224 offset:49152
	ds_read_b128 v[166:169], v224 offset:50176
	ds_read_b128 v[170:173], v224 offset:51200
	ds_read_b128 v[174:177], v224 offset:52224
	ds_read_b128 v[178:181], v224 offset:53248
	ds_read_b128 v[182:185], v224 offset:54272
	ds_read_b128 v[186:189], v224 offset:55296
	ds_read_b128 v[190:193], v224 offset:56320
	global_load_lds_dwordx4 v[242:243], off
	s_add_i32 m0, s26, 0x2000
	s_add_i32 s26, s82, s35
	global_load_lds_dwordx4 v[244:245], off
	s_mov_b32 m0, s26
	s_nop 0
	global_load_lds_dwordx4 v[248:249], off
	s_add_i32 m0, s26, 0x2000
	s_nop 0
	global_load_lds_dwordx4 v[240:241], off
	s_mov_b32 m0, s67
	s_nop 0
	global_load_lds_dwordx4 v[250:251], off
	s_mov_b32 m0, s68
	s_nop 0
	global_load_lds_dwordx4 v[246:247], off
	s_waitcnt vmcnt(8)
	s_waitcnt lgkmcnt(0)
	s_barrier
	s_waitcnt lgkmcnt(0)
	v_mfma_f32_16x16x32_bf16 v[62:65], v[130:133], v[162:165], v[62:65]
	v_mfma_f32_16x16x32_bf16 v[58:61], v[138:141], v[162:165], v[58:61]
	v_mfma_f32_16x16x32_bf16 v[54:57], v[130:133], v[170:173], v[54:57]
	v_mfma_f32_16x16x32_bf16 v[50:53], v[138:141], v[170:173], v[50:53]
	v_mfma_f32_16x16x32_bf16 v[46:49], v[130:133], v[178:181], v[46:49]
	v_mfma_f32_16x16x32_bf16 v[38:41], v[138:141], v[178:181], v[38:41]
	v_mfma_f32_16x16x32_bf16 v[30:33], v[130:133], v[186:189], v[30:33]
	v_mfma_f32_16x16x32_bf16 v[10:13], v[138:141], v[186:189], v[10:13]
	v_mfma_f32_16x16x32_bf16 v[62:65], v[134:137], v[166:169], v[62:65]
	v_mfma_f32_16x16x32_bf16 v[58:61], v[142:145], v[166:169], v[58:61]
	v_mfma_f32_16x16x32_bf16 v[54:57], v[134:137], v[174:177], v[54:57]
	v_mfma_f32_16x16x32_bf16 v[50:53], v[142:145], v[174:177], v[50:53]
	v_mfma_f32_16x16x32_bf16 v[46:49], v[134:137], v[182:185], v[46:49]
	v_mfma_f32_16x16x32_bf16 v[38:41], v[142:145], v[182:185], v[38:41]
	v_mfma_f32_16x16x32_bf16 v[30:33], v[134:137], v[190:193], v[30:33]
	v_mfma_f32_16x16x32_bf16 v[10:13], v[142:145], v[190:193], v[10:13]
	v_mfma_f32_16x16x32_bf16 v[42:45], v[146:149], v[162:165], v[42:45]
	v_mfma_f32_16x16x32_bf16 v[34:37], v[154:157], v[162:165], v[34:37]
	v_mfma_f32_16x16x32_bf16 v[26:29], v[146:149], v[170:173], v[26:29]
	v_mfma_f32_16x16x32_bf16 v[22:25], v[154:157], v[170:173], v[22:25]
	v_mfma_f32_16x16x32_bf16 v[18:21], v[146:149], v[178:181], v[18:21]
	v_mfma_f32_16x16x32_bf16 v[14:17], v[154:157], v[178:181], v[14:17]
	v_mfma_f32_16x16x32_bf16 v[6:9], v[146:149], v[186:189], v[6:9]
	v_mfma_f32_16x16x32_bf16 v[2:5], v[154:157], v[186:189], v[2:5]
	v_mfma_f32_16x16x32_bf16 v[42:45], v[150:153], v[166:169], v[42:45]
	v_mfma_f32_16x16x32_bf16 v[34:37], v[158:161], v[166:169], v[34:37]
	v_mfma_f32_16x16x32_bf16 v[26:29], v[150:153], v[174:177], v[26:29]
	v_mfma_f32_16x16x32_bf16 v[22:25], v[158:161], v[174:177], v[22:25]
	v_mfma_f32_16x16x32_bf16 v[18:21], v[150:153], v[182:185], v[18:21]
	v_mfma_f32_16x16x32_bf16 v[14:17], v[158:161], v[182:185], v[14:17]
	v_mfma_f32_16x16x32_bf16 v[6:9], v[150:153], v[190:193], v[6:9]
	v_mfma_f32_16x16x32_bf16 v[2:5], v[158:161], v[190:193], v[2:5]
	s_barrier
	s_add_i32 s80, s80, 2
	s_add_u32 s74, s74, 0x10000
	s_addc_u32 s75, s75, 0
	s_add_u32 s58, s58, 0x100
	s_addc_u32 s59, s59, 0
	s_cmp_gt_u32 s80, 29
	s_cbranch_scc0 .LBB0_660
	s_and_b64 vcc, exec, s[24:25]
	s_cbranch_vccz .LBB0_663
	s_barrier

.LBB0_783:
	ds_read_b128 v[144:147], v151
	ds_read_b128 v[156:159], v151 offset:1024
	ds_read_b128 v[160:163], v151 offset:2048
	ds_read_b128 v[164:167], v151 offset:3072
	ds_read_b128 v[168:171], v152
	ds_read_b128 v[172:175], v152 offset:1024
	ds_read_b128 v[176:179], v152 offset:2048
	ds_read_b128 v[180:183], v152 offset:3072
	s_add_u32 s26, s62, 0xfff80080
	s_addc_u32 s27, s63, -1
	s_cmp_eq_u32 s85, 28
	s_cselect_b32 s65, s55, s27
	s_cselect_b32 s64, s81, s26
	s_cselect_b32 s27, s53, s84
	s_cselect_b32 s26, s82, s83
	v_lshl_add_u64 v[216:217], s[62:63], 0, v[136:137]
	s_add_i32 m0, s61, 0xc000
	ds_read_b128 v[184:187], v153
	ds_read_b128 v[188:191], v153 offset:1024
	ds_read_b128 v[192:195], v153 offset:2048
	ds_read_b128 v[196:199], v153 offset:3072
	ds_read_b128 v[200:203], v153 offset:4096
	ds_read_b128 v[204:207], v153 offset:5120
	ds_read_b128 v[208:211], v153 offset:6144
	ds_read_b128 v[212:215], v153 offset:7168
	global_load_lds_dwordx4 v[216:217], off
	v_lshl_add_u64 v[216:217], s[62:63], 0, v[138:139]
	s_add_i32 m0, s61, 0xe000
	s_nop 0
	global_load_lds_dwordx4 v[216:217], off
	s_waitcnt vmcnt(8)
	s_waitcnt lgkmcnt(0)
	s_barrier
	s_waitcnt lgkmcnt(0)
	v_mfma_f32_16x16x32_bf16 v[126:129], v[144:147], v[184:187], v[126:129]
	v_mfma_f32_16x16x32_bf16 v[118:121], v[160:163], v[184:187], v[118:121]
	v_lshl_add_u64 v[240:241], s[26:27], 0, v[130:131]
	v_mfma_f32_16x16x32_bf16 v[110:113], v[144:147], v[192:195], v[110:113]
	v_mfma_f32_16x16x32_bf16 v[102:105], v[160:163], v[192:195], v[102:105]
	v_lshl_add_u64 v[242:243], v[240:241], 0, s[6:7]
	v_mfma_f32_16x16x32_bf16 v[94:97], v[144:147], v[200:203], v[94:97]
	v_mfma_f32_16x16x32_bf16 v[86:89], v[160:163], v[200:203], v[86:89]
	v_lshl_add_u64 v[244:245], v[240:241], 0, s[8:9]
	v_mfma_f32_16x16x32_bf16 v[78:81], v[144:147], v[208:211], v[78:81]
	v_mfma_f32_16x16x32_bf16 v[70:73], v[160:163], v[208:211], v[70:73]
	v_lshl_add_u64 v[246:247], s[64:65], 0, v[134:135]
	v_mfma_f32_16x16x32_bf16 v[126:129], v[156:159], v[188:191], v[126:129]
	v_mfma_f32_16x16x32_bf16 v[118:121], v[164:167], v[188:191], v[118:121]
	v_lshl_add_u64 v[248:249], v[240:241], 0, s[10:11]
	v_mfma_f32_16x16x32_bf16 v[110:113], v[156:159], v[196:199], v[110:113]
	v_mfma_f32_16x16x32_bf16 v[102:105], v[164:167], v[196:199], v[102:105]
	v_lshl_add_u64 v[250:251], s[64:65], 0, v[132:133]
	v_mfma_f32_16x16x32_bf16 v[94:97], v[156:159], v[204:207], v[94:97]
	v_mfma_f32_16x16x32_bf16 v[86:89], v[164:167], v[204:207], v[86:89]
	v_mfma_f32_16x16x32_bf16 v[78:81], v[156:159], v[212:215], v[78:81]
	v_mfma_f32_16x16x32_bf16 v[70:73], v[164:167], v[212:215], v[70:73]
	v_mfma_f32_16x16x32_bf16 v[122:125], v[168:171], v[184:187], v[122:125]
	v_mfma_f32_16x16x32_bf16 v[114:117], v[176:179], v[184:187], v[114:117]
	v_mfma_f32_16x16x32_bf16 v[106:109], v[168:171], v[192:195], v[106:109]
	v_mfma_f32_16x16x32_bf16 v[98:101], v[176:179], v[192:195], v[98:101]
	v_mfma_f32_16x16x32_bf16 v[90:93], v[168:171], v[200:203], v[90:93]
	v_mfma_f32_16x16x32_bf16 v[82:85], v[176:179], v[200:203], v[82:85]
	v_mfma_f32_16x16x32_bf16 v[74:77], v[168:171], v[208:211], v[74:77]
	v_mfma_f32_16x16x32_bf16 v[66:69], v[176:179], v[208:211], v[66:69]
	v_mfma_f32_16x16x32_bf16 v[122:125], v[172:175], v[188:191], v[122:125]
	v_mfma_f32_16x16x32_bf16 v[114:117], v[180:183], v[188:191], v[114:117]
	v_mfma_f32_16x16x32_bf16 v[106:109], v[172:175], v[196:199], v[106:109]
	v_mfma_f32_16x16x32_bf16 v[98:101], v[180:183], v[196:199], v[98:101]
	v_mfma_f32_16x16x32_bf16 v[90:93], v[172:175], v[204:207], v[90:93]
	v_mfma_f32_16x16x32_bf16 v[82:85], v[180:183], v[204:207], v[82:85]
	v_mfma_f32_16x16x32_bf16 v[74:77], v[172:175], v[212:215], v[74:77]
	v_mfma_f32_16x16x32_bf16 v[66:69], v[180:183], v[212:215], v[66:69]
	s_barrier
	s_add_i32 s26, s73, s35
	s_mov_b32 m0, s26
	ds_read_b128 v[184:187], v153 offset:16384
	ds_read_b128 v[188:191], v153 offset:17408
	ds_read_b128 v[192:195], v153 offset:18432
	ds_read_b128 v[196:199], v153 offset:19456
	ds_read_b128 v[200:203], v153 offset:20480
	ds_read_b128 v[204:207], v153 offset:21504
	ds_read_b128 v[208:211], v153 offset:22528
	ds_read_b128 v[212:215], v153 offset:23552
	global_load_lds_dwordx4 v[240:241], off
	s_add_i32 m0, s26, 0x2000
	s_add_i32 s26, s74, s35
	global_load_lds_dwordx4 v[242:243], off
	s_mov_b32 m0, s26
	s_nop 0
	global_load_lds_dwordx4 v[244:245], off
	s_add_i32 m0, s26, 0x2000
	s_nop 0
	global_load_lds_dwordx4 v[248:249], off
	s_mov_b32 m0, s61
	s_nop 0
	global_load_lds_dwordx4 v[250:251], off
	s_mov_b32 m0, s66
	s_nop 0
	global_load_lds_dwordx4 v[246:247], off
	s_waitcnt vmcnt(8)
	s_waitcnt lgkmcnt(0)
	s_barrier
	s_waitcnt lgkmcnt(0)
	v_mfma_f32_16x16x32_bf16 v[62:65], v[144:147], v[184:187], v[62:65]
	v_mfma_f32_16x16x32_bf16 v[54:57], v[160:163], v[184:187], v[54:57]
	v_mfma_f32_16x16x32_bf16 v[46:49], v[144:147], v[192:195], v[46:49]
	v_mfma_f32_16x16x32_bf16 v[38:41], v[160:163], v[192:195], v[38:41]
	v_mfma_f32_16x16x32_bf16 v[30:33], v[144:147], v[200:203], v[30:33]
	v_mfma_f32_16x16x32_bf16 v[22:25], v[160:163], v[200:203], v[22:25]
	v_mfma_f32_16x16x32_bf16 v[14:17], v[144:147], v[208:211], v[14:17]
	v_mfma_f32_16x16x32_bf16 v[6:9], v[160:163], v[208:211], v[6:9]
	v_mfma_f32_16x16x32_bf16 v[62:65], v[156:159], v[188:191], v[62:65]
	v_mfma_f32_16x16x32_bf16 v[54:57], v[164:167], v[188:191], v[54:57]
	v_mfma_f32_16x16x32_bf16 v[46:49], v[156:159], v[196:199], v[46:49]
	v_mfma_f32_16x16x32_bf16 v[38:41], v[164:167], v[196:199], v[38:41]
	v_mfma_f32_16x16x32_bf16 v[30:33], v[156:159], v[204:207], v[30:33]
	v_mfma_f32_16x16x32_bf16 v[22:25], v[164:167], v[204:207], v[22:25]
	v_mfma_f32_16x16x32_bf16 v[14:17], v[156:159], v[212:215], v[14:17]
	v_mfma_f32_16x16x32_bf16 v[6:9], v[164:167], v[212:215], v[6:9]
	v_mfma_f32_16x16x32_bf16 v[58:61], v[168:171], v[184:187], v[58:61]
	v_mfma_f32_16x16x32_bf16 v[50:53], v[176:179], v[184:187], v[50:53]
	v_mfma_f32_16x16x32_bf16 v[42:45], v[168:171], v[192:195], v[42:45]
	v_mfma_f32_16x16x32_bf16 v[34:37], v[176:179], v[192:195], v[34:37]
	v_mfma_f32_16x16x32_bf16 v[26:29], v[168:171], v[200:203], v[26:29]
	v_mfma_f32_16x16x32_bf16 v[18:21], v[176:179], v[200:203], v[18:21]
	v_mfma_f32_16x16x32_bf16 v[10:13], v[168:171], v[208:211], v[10:13]
	v_mfma_f32_16x16x32_bf16 v[2:5], v[176:179], v[208:211], v[2:5]
	v_mfma_f32_16x16x32_bf16 v[58:61], v[172:175], v[188:191], v[58:61]
	v_mfma_f32_16x16x32_bf16 v[50:53], v[180:183], v[188:191], v[50:53]
	v_mfma_f32_16x16x32_bf16 v[42:45], v[172:175], v[196:199], v[42:45]
	v_mfma_f32_16x16x32_bf16 v[34:37], v[180:183], v[196:199], v[34:37]
	v_mfma_f32_16x16x32_bf16 v[26:29], v[172:175], v[204:207], v[26:29]
	v_mfma_f32_16x16x32_bf16 v[18:21], v[180:183], v[204:207], v[18:21]
	v_mfma_f32_16x16x32_bf16 v[10:13], v[172:175], v[212:215], v[10:13]
	v_mfma_f32_16x16x32_bf16 v[2:5], v[180:183], v[212:215], v[2:5]
	s_barrier
	s_add_i32 s86, 0, 0x18000
	v_add_u32_e32 v155, s86, v149
	s_add_i32 s87, 0, 0x1c000
	ds_read_b128 v[144:147], v155
	ds_read_b128 v[156:159], v155 offset:1024
	ds_read_b128 v[160:163], v155 offset:2048
	ds_read_b128 v[164:167], v155 offset:3072
	v_add_u32_e32 v155, s87, v149
	ds_read_b128 v[168:171], v155
	ds_read_b128 v[172:175], v155 offset:1024
	ds_read_b128 v[176:179], v155 offset:2048
	ds_read_b128 v[180:183], v155 offset:3072
	s_add_u32 s26, s64, 0x80000
	s_addc_u32 s27, s65, 0
	s_mov_b32 m0, s67
	v_lshl_add_u64 v[224:225], s[26:27], 0, v[132:133]
	ds_read_b128 v[184:187], v153 offset:32768
	ds_read_b128 v[188:191], v153 offset:33792
	ds_read_b128 v[192:195], v153 offset:34816
	ds_read_b128 v[196:199], v153 offset:35840
	ds_read_b128 v[200:203], v153 offset:36864
	ds_read_b128 v[204:207], v153 offset:37888
	ds_read_b128 v[208:211], v153 offset:38912
	ds_read_b128 v[212:215], v153 offset:39936
	global_load_lds_dwordx4 v[224:225], off
	v_lshl_add_u64 v[224:225], s[26:27], 0, v[134:135]
	s_mov_b32 m0, s68
	s_nop 0
	global_load_lds_dwordx4 v[224:225], off
	s_waitcnt vmcnt(8)
	s_waitcnt lgkmcnt(0)
	s_barrier
	s_waitcnt lgkmcnt(0)
	v_mfma_f32_16x16x32_bf16 v[126:129], v[144:147], v[184:187], v[126:129]
	v_mfma_f32_16x16x32_bf16 v[118:121], v[160:163], v[184:187], v[118:121]
	v_lshl_add_u64 v[242:243], v[240:241], 0, s[16:17]
	v_mfma_f32_16x16x32_bf16 v[110:113], v[144:147], v[192:195], v[110:113]
	v_mfma_f32_16x16x32_bf16 v[102:105], v[160:163], v[192:195], v[102:105]
	v_lshl_add_u64 v[244:245], v[240:241], 0, s[18:19]
	v_mfma_f32_16x16x32_bf16 v[94:97], v[144:147], v[200:203], v[94:97]
	v_mfma_f32_16x16x32_bf16 v[86:89], v[160:163], v[200:203], v[86:89]
	v_lshl_add_u64 v[248:249], v[240:241], 0, s[22:23]
	v_mfma_f32_16x16x32_bf16 v[78:81], v[144:147], v[208:211], v[78:81]
	v_mfma_f32_16x16x32_bf16 v[70:73], v[160:163], v[208:211], v[70:73]
	v_lshl_add_u64 v[240:241], v[240:241], 0, s[24:25]
	v_mfma_f32_16x16x32_bf16 v[126:129], v[156:159], v[188:191], v[126:129]
	v_mfma_f32_16x16x32_bf16 v[118:121], v[164:167], v[188:191], v[118:121]
	v_lshl_add_u64 v[250:251], v[250:251], 0, s[20:21]
	v_mfma_f32_16x16x32_bf16 v[110:113], v[156:159], v[196:199], v[110:113]
	v_mfma_f32_16x16x32_bf16 v[102:105], v[164:167], v[196:199], v[102:105]
	v_lshl_add_u64 v[246:247], v[246:247], 0, s[20:21]
	v_mfma_f32_16x16x32_bf16 v[94:97], v[156:159], v[204:207], v[94:97]
	v_mfma_f32_16x16x32_bf16 v[86:89], v[164:167], v[204:207], v[86:89]
	v_mfma_f32_16x16x32_bf16 v[78:81], v[156:159], v[212:215], v[78:81]
	v_mfma_f32_16x16x32_bf16 v[70:73], v[164:167], v[212:215], v[70:73]
	v_mfma_f32_16x16x32_bf16 v[122:125], v[168:171], v[184:187], v[122:125]
	v_mfma_f32_16x16x32_bf16 v[114:117], v[176:179], v[184:187], v[114:117]
	v_mfma_f32_16x16x32_bf16 v[106:109], v[168:171], v[192:195], v[106:109]
	v_mfma_f32_16x16x32_bf16 v[98:101], v[176:179], v[192:195], v[98:101]
	v_mfma_f32_16x16x32_bf16 v[90:93], v[168:171], v[200:203], v[90:93]
	v_mfma_f32_16x16x32_bf16 v[82:85], v[176:179], v[200:203], v[82:85]
	v_mfma_f32_16x16x32_bf16 v[74:77], v[168:171], v[208:211], v[74:77]
	v_mfma_f32_16x16x32_bf16 v[66:69], v[176:179], v[208:211], v[66:69]
	v_mfma_f32_16x16x32_bf16 v[122:125], v[172:175], v[188:191], v[122:125]
	v_mfma_f32_16x16x32_bf16 v[114:117], v[180:183], v[188:191], v[114:117]
	v_mfma_f32_16x16x32_bf16 v[106:109], v[172:175], v[196:199], v[106:109]
	v_mfma_f32_16x16x32_bf16 v[98:101], v[180:183], v[196:199], v[98:101]
	v_mfma_f32_16x16x32_bf16 v[90:93], v[172:175], v[204:207], v[90:93]
	v_mfma_f32_16x16x32_bf16 v[82:85], v[180:183], v[204:207], v[82:85]
	v_mfma_f32_16x16x32_bf16 v[74:77], v[172:175], v[212:215], v[74:77]
	v_mfma_f32_16x16x32_bf16 v[66:69], v[180:183], v[212:215], v[66:69]
	s_barrier
	s_add_i32 s26, s86, s35
	s_mov_b32 m0, s26
	ds_read_b128 v[184:187], v153 offset:49152
	ds_read_b128 v[188:191], v153 offset:50176
	ds_read_b128 v[192:195], v153 offset:51200
	ds_read_b128 v[196:199], v153 offset:52224
	ds_read_b128 v[200:203], v153 offset:53248
	ds_read_b128 v[204:207], v153 offset:54272
	ds_read_b128 v[208:211], v153 offset:55296
	ds_read_b128 v[212:215], v153 offset:56320
	global_load_lds_dwordx4 v[242:243], off
	s_add_i32 m0, s26, 0x2000
	s_add_i32 s26, s87, s35
	global_load_lds_dwordx4 v[244:245], off
	s_mov_b32 m0, s26
	s_nop 0
	global_load_lds_dwordx4 v[248:249], off
	s_add_i32 m0, s26, 0x2000
	s_nop 0
	global_load_lds_dwordx4 v[240:241], off
	s_mov_b32 m0, s70
	s_nop 0
	global_load_lds_dwordx4 v[250:251], off
	s_mov_b32 m0, s71
	s_nop 0
	global_load_lds_dwordx4 v[246:247], off
	s_waitcnt vmcnt(8)
	s_waitcnt lgkmcnt(0)
	s_barrier
	s_waitcnt lgkmcnt(0)
	v_mfma_f32_16x16x32_bf16 v[62:65], v[144:147], v[184:187], v[62:65]
	v_mfma_f32_16x16x32_bf16 v[54:57], v[160:163], v[184:187], v[54:57]
	v_mfma_f32_16x16x32_bf16 v[46:49], v[144:147], v[192:195], v[46:49]
	v_mfma_f32_16x16x32_bf16 v[38:41], v[160:163], v[192:195], v[38:41]
	v_mfma_f32_16x16x32_bf16 v[30:33], v[144:147], v[200:203], v[30:33]
	v_mfma_f32_16x16x32_bf16 v[22:25], v[160:163], v[200:203], v[22:25]
	v_mfma_f32_16x16x32_bf16 v[14:17], v[144:147], v[208:211], v[14:17]
	v_mfma_f32_16x16x32_bf16 v[6:9], v[160:163], v[208:211], v[6:9]
	v_mfma_f32_16x16x32_bf16 v[62:65], v[156:159], v[188:191], v[62:65]
	v_mfma_f32_16x16x32_bf16 v[54:57], v[164:167], v[188:191], v[54:57]
	v_mfma_f32_16x16x32_bf16 v[46:49], v[156:159], v[196:199], v[46:49]
	v_mfma_f32_16x16x32_bf16 v[38:41], v[164:167], v[196:199], v[38:41]
	v_mfma_f32_16x16x32_bf16 v[30:33], v[156:159], v[204:207], v[30:33]
	v_mfma_f32_16x16x32_bf16 v[22:25], v[164:167], v[204:207], v[22:25]
	v_mfma_f32_16x16x32_bf16 v[14:17], v[156:159], v[212:215], v[14:17]
	v_mfma_f32_16x16x32_bf16 v[6:9], v[164:167], v[212:215], v[6:9]
	v_mfma_f32_16x16x32_bf16 v[58:61], v[168:171], v[184:187], v[58:61]
	v_mfma_f32_16x16x32_bf16 v[50:53], v[176:179], v[184:187], v[50:53]
	v_mfma_f32_16x16x32_bf16 v[42:45], v[168:171], v[192:195], v[42:45]
	v_mfma_f32_16x16x32_bf16 v[34:37], v[176:179], v[192:195], v[34:37]
	v_mfma_f32_16x16x32_bf16 v[26:29], v[168:171], v[200:203], v[26:29]
	v_mfma_f32_16x16x32_bf16 v[18:21], v[176:179], v[200:203], v[18:21]
	v_mfma_f32_16x16x32_bf16 v[10:13], v[168:171], v[208:211], v[10:13]
	v_mfma_f32_16x16x32_bf16 v[2:5], v[176:179], v[208:211], v[2:5]
	v_mfma_f32_16x16x32_bf16 v[58:61], v[172:175], v[188:191], v[58:61]
	v_mfma_f32_16x16x32_bf16 v[50:53], v[180:183], v[188:191], v[50:53]
	v_mfma_f32_16x16x32_bf16 v[42:45], v[172:175], v[196:199], v[42:45]
	v_mfma_f32_16x16x32_bf16 v[34:37], v[180:183], v[196:199], v[34:37]
	v_mfma_f32_16x16x32_bf16 v[26:29], v[172:175], v[204:207], v[26:29]
	v_mfma_f32_16x16x32_bf16 v[18:21], v[180:183], v[204:207], v[18:21]
	v_mfma_f32_16x16x32_bf16 v[10:13], v[172:175], v[212:215], v[10:13]
	v_mfma_f32_16x16x32_bf16 v[2:5], v[180:183], v[212:215], v[2:5]
	s_barrier
	s_add_i32 s85, s85, 2
	s_add_u32 s83, s83, 0x10000
	s_addc_u32 s84, s84, 0
	s_add_u32 s62, s62, 0x100
	s_addc_u32 s63, s63, 0
	s_cmp_gt_u32 s85, 29
	s_cbranch_scc0 .LBB0_783
	s_and_b64 vcc, exec, s[40:41]
	s_cbranch_vccz .LBB0_786
	s_barrier

.LBB0_858:
	ds_read_b128 v[26:29], v185
	ds_read_b128 v[30:33], v185 offset:1024
	ds_read_b128 v[18:21], v185 offset:2048
	ds_read_b128 v[22:25], v185 offset:3072
	ds_read_b128 v[10:13], v186
	ds_read_b128 v[14:17], v186 offset:1024
	ds_read_b128 v[2:5], v186 offset:2048
	ds_read_b128 v[6:9], v186 offset:3072
	s_add_u32 s26, s50, 0xfff50080
	s_addc_u32 s27, s51, -1
	s_cmp_eq_u32 s74, 40
	s_cselect_b32 s53, s5, s27
	s_cselect_b32 s52, s4, s26
	s_cselect_b32 s55, s45, s73
	s_cselect_b32 s54, s44, s72
	v_lshl_add_u64 v[176:177], s[50:51], 0, v[168:169]
	s_add_i32 m0, s59, 0xc000
	ds_read_b128 v[190:193], v187
	ds_read_b128 v[194:197], v187 offset:1024
	ds_read_b128 v[198:201], v187 offset:2048
	ds_read_b128 v[202:205], v187 offset:3072
	ds_read_b128 v[206:209], v187 offset:4096
	ds_read_b128 v[210:213], v187 offset:5120
	ds_read_b128 v[220:223], v187 offset:6144
	ds_read_b128 v[224:227], v187 offset:7168
	global_load_lds_dwordx4 v[176:177], off
	v_lshl_add_u64 v[176:177], s[50:51], 0, v[170:171]
	s_add_i32 m0, s59, 0xe000
	s_nop 0
	global_load_lds_dwordx4 v[176:177], off
	s_waitcnt vmcnt(8)
	s_waitcnt lgkmcnt(0)
	s_barrier
	s_waitcnt lgkmcnt(0)
	v_mfma_scale_f32_16x16x128_f8f6f4 v[158:161], v[26:33], v[190:197], v[158:161], v188, v189 op_sel_hi:[0,0,0]
	v_mfma_scale_f32_16x16x128_f8f6f4 v[154:157], v[18:25], v[190:197], v[154:157], v188, v189 op_sel_hi:[0,0,0]
	v_lshl_add_u64 v[240:241], s[54:55], 0, v[162:163]
	v_mfma_scale_f32_16x16x128_f8f6f4 v[150:153], v[26:33], v[198:205], v[150:153], v188, v189 op_sel_hi:[0,0,0]
	v_mfma_scale_f32_16x16x128_f8f6f4 v[146:149], v[18:25], v[198:205], v[146:149], v188, v189 op_sel_hi:[0,0,0]
	v_lshl_add_u64 v[242:243], v[240:241], 0, s[8:9]
	v_mfma_scale_f32_16x16x128_f8f6f4 v[138:141], v[26:33], v[206:213], v[138:141], v188, v189 op_sel_hi:[0,0,0]
	v_mfma_scale_f32_16x16x128_f8f6f4 v[130:133], v[18:25], v[206:213], v[130:133], v188, v189 op_sel_hi:[0,0,0]
	v_lshl_add_u64 v[244:245], v[240:241], 0, s[10:11]
	v_mfma_scale_f32_16x16x128_f8f6f4 v[122:125], v[26:33], v[220:227], v[122:125], v188, v189 op_sel_hi:[0,0,0]
	v_mfma_scale_f32_16x16x128_f8f6f4 v[114:117], v[18:25], v[220:227], v[114:117], v188, v189 op_sel_hi:[0,0,0]
	v_lshl_add_u64 v[246:247], s[52:53], 0, v[166:167]
	v_mfma_scale_f32_16x16x128_f8f6f4 v[142:145], v[10:17], v[190:197], v[142:145], v188, v189 op_sel_hi:[0,0,0]
	v_mfma_scale_f32_16x16x128_f8f6f4 v[134:137], v[2:9], v[190:197], v[134:137], v188, v189 op_sel_hi:[0,0,0]
	v_lshl_add_u64 v[248:249], v[240:241], 0, s[12:13]
	v_mfma_scale_f32_16x16x128_f8f6f4 v[126:129], v[10:17], v[198:205], v[126:129], v188, v189 op_sel_hi:[0,0,0]
	v_mfma_scale_f32_16x16x128_f8f6f4 v[118:121], v[2:9], v[198:205], v[118:121], v188, v189 op_sel_hi:[0,0,0]
	v_lshl_add_u64 v[250:251], s[52:53], 0, v[164:165]
	v_mfma_scale_f32_16x16x128_f8f6f4 v[110:113], v[10:17], v[206:213], v[110:113], v188, v189 op_sel_hi:[0,0,0]
	v_mfma_scale_f32_16x16x128_f8f6f4 v[106:109], v[2:9], v[206:213], v[106:109], v188, v189 op_sel_hi:[0,0,0]
	v_mfma_scale_f32_16x16x128_f8f6f4 v[102:105], v[10:17], v[220:227], v[102:105], v188, v189 op_sel_hi:[0,0,0]
	v_mfma_scale_f32_16x16x128_f8f6f4 v[98:101], v[2:9], v[220:227], v[98:101], v188, v189 op_sel_hi:[0,0,0]
	s_barrier
	s_add_i32 s26, s67, s57
	s_mov_b32 m0, s26
	ds_read_b128 v[190:193], v187 offset:16384
	ds_read_b128 v[194:197], v187 offset:17408
	ds_read_b128 v[198:201], v187 offset:18432
	ds_read_b128 v[202:205], v187 offset:19456
	ds_read_b128 v[206:209], v187 offset:20480
	ds_read_b128 v[210:213], v187 offset:21504
	ds_read_b128 v[220:223], v187 offset:22528
	ds_read_b128 v[224:227], v187 offset:23552
	global_load_lds_dwordx4 v[240:241], off
	s_add_i32 m0, s26, 0x2000
	s_add_i32 s26, s68, s57
	global_load_lds_dwordx4 v[242:243], off
	s_mov_b32 m0, s26
	s_nop 0
	global_load_lds_dwordx4 v[244:245], off
	s_add_i32 m0, s26, 0x2000
	s_nop 0
	global_load_lds_dwordx4 v[248:249], off
	s_mov_b32 m0, s59
	s_nop 0
	global_load_lds_dwordx4 v[250:251], off
	s_mov_b32 m0, s60
	s_nop 0
	global_load_lds_dwordx4 v[246:247], off
	s_waitcnt vmcnt(8)
	s_waitcnt lgkmcnt(0)
	s_barrier
	s_waitcnt lgkmcnt(0)
	v_mfma_scale_f32_16x16x128_f8f6f4 v[94:97], v[26:33], v[190:197], v[94:97], v188, v189 op_sel_hi:[0,0,0]
	v_mfma_scale_f32_16x16x128_f8f6f4 v[90:93], v[18:25], v[190:197], v[90:93], v188, v189 op_sel_hi:[0,0,0]
	v_mfma_scale_f32_16x16x128_f8f6f4 v[86:89], v[26:33], v[198:205], v[86:89], v188, v189 op_sel_hi:[0,0,0]
	v_mfma_scale_f32_16x16x128_f8f6f4 v[78:81], v[18:25], v[198:205], v[78:81], v188, v189 op_sel_hi:[0,0,0]
	v_mfma_scale_f32_16x16x128_f8f6f4 v[70:73], v[26:33], v[206:213], v[70:73], v188, v189 op_sel_hi:[0,0,0]
	v_mfma_scale_f32_16x16x128_f8f6f4 v[62:65], v[18:25], v[206:213], v[62:65], v188, v189 op_sel_hi:[0,0,0]
	v_mfma_scale_f32_16x16x128_f8f6f4 v[54:57], v[26:33], v[220:227], v[54:57], v188, v189 op_sel_hi:[0,0,0]
	v_mfma_scale_f32_16x16x128_f8f6f4 v[46:49], v[18:25], v[220:227], v[46:49], v188, v189 op_sel_hi:[0,0,0]
	v_mfma_scale_f32_16x16x128_f8f6f4 v[82:85], v[10:17], v[190:197], v[82:85], v188, v189 op_sel_hi:[0,0,0]
	v_mfma_scale_f32_16x16x128_f8f6f4 v[74:77], v[2:9], v[190:197], v[74:77], v188, v189 op_sel_hi:[0,0,0]
	v_mfma_scale_f32_16x16x128_f8f6f4 v[66:69], v[10:17], v[198:205], v[66:69], v188, v189 op_sel_hi:[0,0,0]
	v_mfma_scale_f32_16x16x128_f8f6f4 v[58:61], v[2:9], v[198:205], v[58:61], v188, v189 op_sel_hi:[0,0,0]
	v_mfma_scale_f32_16x16x128_f8f6f4 v[50:53], v[10:17], v[206:213], v[50:53], v188, v189 op_sel_hi:[0,0,0]
	v_mfma_scale_f32_16x16x128_f8f6f4 v[42:45], v[2:9], v[206:213], v[42:45], v188, v189 op_sel_hi:[0,0,0]
	v_mfma_scale_f32_16x16x128_f8f6f4 v[38:41], v[10:17], v[220:227], v[38:41], v188, v189 op_sel_hi:[0,0,0]
	v_mfma_scale_f32_16x16x128_f8f6f4 v[34:37], v[2:9], v[220:227], v[34:37], v188, v189 op_sel_hi:[0,0,0]
	s_barrier
	s_add_i32 s54, 0, 0x18000
	s_add_i32 s55, 0, 0x1c000
	v_add_u32_e32 v14, s54, v183
	v_add_u32_e32 v30, s55, v183
	ds_read_b128 v[2:5], v14
	ds_read_b128 v[6:9], v14 offset:1024
	ds_read_b128 v[10:13], v14 offset:2048
	ds_read_b128 v[14:17], v14 offset:3072
	ds_read_b128 v[18:21], v30
	ds_read_b128 v[22:25], v30 offset:1024
	ds_read_b128 v[26:29], v30 offset:2048
	ds_read_b128 v[30:33], v30 offset:3072
	s_add_u32 s26, s52, 0xb0000
	s_addc_u32 s27, s53, 0
	s_mov_b32 m0, s61
	v_lshl_add_u64 v[214:215], s[26:27], 0, v[164:165]
	ds_read_b128 v[190:193], v187 offset:32768
	ds_read_b128 v[194:197], v187 offset:33792
	ds_read_b128 v[198:201], v187 offset:34816
	ds_read_b128 v[202:205], v187 offset:35840
	ds_read_b128 v[206:209], v187 offset:36864
	ds_read_b128 v[210:213], v187 offset:37888
	ds_read_b128 v[220:223], v187 offset:38912
	ds_read_b128 v[224:227], v187 offset:39936
	global_load_lds_dwordx4 v[214:215], off
	v_lshl_add_u64 v[214:215], s[26:27], 0, v[166:167]
	s_mov_b32 m0, s62
	s_nop 0
	global_load_lds_dwordx4 v[214:215], off
	s_waitcnt vmcnt(8)
	s_waitcnt lgkmcnt(0)
	s_barrier
	s_waitcnt lgkmcnt(0)
	v_mfma_scale_f32_16x16x128_f8f6f4 v[158:161], v[2:9], v[190:197], v[158:161], v188, v189 op_sel_hi:[0,0,0]
	v_mfma_scale_f32_16x16x128_f8f6f4 v[154:157], v[10:17], v[190:197], v[154:157], v188, v189 op_sel_hi:[0,0,0]
	v_lshl_add_u64 v[242:243], v[240:241], 0, s[16:17]
	v_mfma_scale_f32_16x16x128_f8f6f4 v[150:153], v[2:9], v[198:205], v[150:153], v188, v189 op_sel_hi:[0,0,0]
	v_mfma_scale_f32_16x16x128_f8f6f4 v[146:149], v[10:17], v[198:205], v[146:149], v188, v189 op_sel_hi:[0,0,0]
	v_lshl_add_u64 v[244:245], v[240:241], 0, s[18:19]
	v_mfma_scale_f32_16x16x128_f8f6f4 v[138:141], v[2:9], v[206:213], v[138:141], v188, v189 op_sel_hi:[0,0,0]
	v_mfma_scale_f32_16x16x128_f8f6f4 v[130:133], v[10:17], v[206:213], v[130:133], v188, v189 op_sel_hi:[0,0,0]
	v_lshl_add_u64 v[248:249], v[240:241], 0, s[22:23]
	v_mfma_scale_f32_16x16x128_f8f6f4 v[122:125], v[2:9], v[220:227], v[122:125], v188, v189 op_sel_hi:[0,0,0]
	v_mfma_scale_f32_16x16x128_f8f6f4 v[114:117], v[10:17], v[220:227], v[114:117], v188, v189 op_sel_hi:[0,0,0]
	v_lshl_add_u64 v[240:241], v[240:241], 0, s[24:25]
	v_mfma_scale_f32_16x16x128_f8f6f4 v[142:145], v[18:25], v[190:197], v[142:145], v188, v189 op_sel_hi:[0,0,0]
	v_mfma_scale_f32_16x16x128_f8f6f4 v[134:137], v[26:33], v[190:197], v[134:137], v188, v189 op_sel_hi:[0,0,0]
	v_lshl_add_u64 v[250:251], v[250:251], 0, s[20:21]
	v_mfma_scale_f32_16x16x128_f8f6f4 v[126:129], v[18:25], v[198:205], v[126:129], v188, v189 op_sel_hi:[0,0,0]
	v_mfma_scale_f32_16x16x128_f8f6f4 v[118:121], v[26:33], v[198:205], v[118:121], v188, v189 op_sel_hi:[0,0,0]
	v_lshl_add_u64 v[246:247], v[246:247], 0, s[20:21]
	v_mfma_scale_f32_16x16x128_f8f6f4 v[110:113], v[18:25], v[206:213], v[110:113], v188, v189 op_sel_hi:[0,0,0]
	v_mfma_scale_f32_16x16x128_f8f6f4 v[106:109], v[26:33], v[206:213], v[106:109], v188, v189 op_sel_hi:[0,0,0]
	v_mfma_scale_f32_16x16x128_f8f6f4 v[102:105], v[18:25], v[220:227], v[102:105], v188, v189 op_sel_hi:[0,0,0]
	v_mfma_scale_f32_16x16x128_f8f6f4 v[98:101], v[26:33], v[220:227], v[98:101], v188, v189 op_sel_hi:[0,0,0]
	s_barrier
	s_add_i32 s26, s54, s57
	s_mov_b32 m0, s26
	ds_read_b128 v[190:193], v187 offset:49152
	ds_read_b128 v[194:197], v187 offset:50176
	ds_read_b128 v[198:201], v187 offset:51200
	ds_read_b128 v[202:205], v187 offset:52224
	ds_read_b128 v[206:209], v187 offset:53248
	ds_read_b128 v[210:213], v187 offset:54272
	ds_read_b128 v[220:223], v187 offset:55296
	ds_read_b128 v[224:227], v187 offset:56320
	global_load_lds_dwordx4 v[242:243], off
	s_add_i32 m0, s26, 0x2000
	s_add_i32 s26, s55, s57
	global_load_lds_dwordx4 v[244:245], off
	s_mov_b32 m0, s26
	s_nop 0
	global_load_lds_dwordx4 v[248:249], off
	s_add_i32 m0, s26, 0x2000
	s_nop 0
	global_load_lds_dwordx4 v[240:241], off
	s_mov_b32 m0, s64
	s_nop 0
	global_load_lds_dwordx4 v[250:251], off
	s_mov_b32 m0, s65
	s_nop 0
	global_load_lds_dwordx4 v[246:247], off
	s_waitcnt vmcnt(8)
	s_waitcnt lgkmcnt(0)
	s_barrier
	s_waitcnt lgkmcnt(0)
	v_mfma_scale_f32_16x16x128_f8f6f4 v[94:97], v[2:9], v[190:197], v[94:97], v188, v189 op_sel_hi:[0,0,0]
	v_mfma_scale_f32_16x16x128_f8f6f4 v[90:93], v[10:17], v[190:197], v[90:93], v188, v189 op_sel_hi:[0,0,0]
	v_mfma_scale_f32_16x16x128_f8f6f4 v[86:89], v[2:9], v[198:205], v[86:89], v188, v189 op_sel_hi:[0,0,0]
	v_mfma_scale_f32_16x16x128_f8f6f4 v[78:81], v[10:17], v[198:205], v[78:81], v188, v189 op_sel_hi:[0,0,0]
	v_mfma_scale_f32_16x16x128_f8f6f4 v[70:73], v[2:9], v[206:213], v[70:73], v188, v189 op_sel_hi:[0,0,0]
	v_mfma_scale_f32_16x16x128_f8f6f4 v[62:65], v[10:17], v[206:213], v[62:65], v188, v189 op_sel_hi:[0,0,0]
	v_mfma_scale_f32_16x16x128_f8f6f4 v[54:57], v[2:9], v[220:227], v[54:57], v188, v189 op_sel_hi:[0,0,0]
	v_mfma_scale_f32_16x16x128_f8f6f4 v[46:49], v[10:17], v[220:227], v[46:49], v188, v189 op_sel_hi:[0,0,0]
	v_mfma_scale_f32_16x16x128_f8f6f4 v[82:85], v[18:25], v[190:197], v[82:85], v188, v189 op_sel_hi:[0,0,0]
	v_mfma_scale_f32_16x16x128_f8f6f4 v[74:77], v[26:33], v[190:197], v[74:77], v188, v189 op_sel_hi:[0,0,0]
	v_mfma_scale_f32_16x16x128_f8f6f4 v[66:69], v[18:25], v[198:205], v[66:69], v188, v189 op_sel_hi:[0,0,0]
	v_mfma_scale_f32_16x16x128_f8f6f4 v[58:61], v[26:33], v[198:205], v[58:61], v188, v189 op_sel_hi:[0,0,0]
	v_mfma_scale_f32_16x16x128_f8f6f4 v[50:53], v[18:25], v[206:213], v[50:53], v188, v189 op_sel_hi:[0,0,0]
	v_mfma_scale_f32_16x16x128_f8f6f4 v[42:45], v[26:33], v[206:213], v[42:45], v188, v189 op_sel_hi:[0,0,0]
	v_mfma_scale_f32_16x16x128_f8f6f4 v[38:41], v[18:25], v[220:227], v[38:41], v188, v189 op_sel_hi:[0,0,0]
	v_mfma_scale_f32_16x16x128_f8f6f4 v[34:37], v[26:33], v[220:227], v[34:37], v188, v189 op_sel_hi:[0,0,0]
	s_barrier
	s_add_i32 s74, s74, 2
	s_add_u32 s72, s72, 0x10000
	s_addc_u32 s73, s73, 0
	s_add_u32 s50, s50, 0x100
	s_addc_u32 s51, s51, 0
	s_cmp_gt_u32 s74, 41
	s_cbranch_scc0 .LBB0_858
	s_and_b64 vcc, exec, s[40:41]
	s_cbranch_vccz .LBB0_861
	s_barrier

.LBB0_985:
	ds_read_b128 v[26:29], v185
	ds_read_b128 v[30:33], v185 offset:1024
	ds_read_b128 v[18:21], v185 offset:2048
	ds_read_b128 v[22:25], v185 offset:3072
	ds_read_b128 v[10:13], v186
	ds_read_b128 v[14:17], v186 offset:1024
	ds_read_b128 v[2:5], v186 offset:2048
	ds_read_b128 v[6:9], v186 offset:3072
	s_add_u32 s26, s56, 0xfffc0080
	s_addc_u32 s27, s57, -1
	s_cmp_eq_u32 s80, 12
	s_cselect_b32 s59, s45, s27
	s_cselect_b32 s58, s72, s26
	s_cselect_b32 s61, s41, s75
	s_cselect_b32 s60, s73, s74
	v_lshl_add_u64 v[176:177], s[56:57], 0, v[168:169]
	s_add_i32 m0, s55, 0xc000
	ds_read_b128 v[192:195], v187
	ds_read_b128 v[196:199], v187 offset:1024
	ds_read_b128 v[200:203], v187 offset:2048
	ds_read_b128 v[204:207], v187 offset:3072
	ds_read_b128 v[208:211], v187 offset:4096
	ds_read_b128 v[212:215], v187 offset:5120
	ds_read_b128 v[220:223], v187 offset:6144
	ds_read_b128 v[224:227], v187 offset:7168
	global_load_lds_dwordx4 v[176:177], off
	v_lshl_add_u64 v[176:177], s[56:57], 0, v[170:171]
	s_add_i32 m0, s55, 0xe000
	s_nop 0
	global_load_lds_dwordx4 v[176:177], off
	s_waitcnt vmcnt(8)
	s_waitcnt lgkmcnt(0)
	s_barrier
	s_waitcnt lgkmcnt(0)
	v_mfma_scale_f32_16x16x128_f8f6f4 v[158:161], v[26:33], v[192:199], v[158:161], v188, v189 op_sel_hi:[0,0,0]
	v_mfma_scale_f32_16x16x128_f8f6f4 v[154:157], v[18:25], v[192:199], v[154:157], v188, v189 op_sel_hi:[0,0,0]
	v_lshl_add_u64 v[240:241], s[60:61], 0, v[162:163]
	v_mfma_scale_f32_16x16x128_f8f6f4 v[146:149], v[26:33], v[200:207], v[146:149], v188, v189 op_sel_hi:[0,0,0]
	v_mfma_scale_f32_16x16x128_f8f6f4 v[138:141], v[18:25], v[200:207], v[138:141], v188, v189 op_sel_hi:[0,0,0]
	v_lshl_add_u64 v[242:243], v[240:241], 0, s[6:7]
	v_mfma_scale_f32_16x16x128_f8f6f4 v[130:133], v[26:33], v[208:215], v[130:133], v188, v189 op_sel_hi:[0,0,0]
	v_mfma_scale_f32_16x16x128_f8f6f4 v[122:125], v[18:25], v[208:215], v[122:125], v188, v189 op_sel_hi:[0,0,0]
	v_lshl_add_u64 v[244:245], v[240:241], 0, s[8:9]
	v_mfma_scale_f32_16x16x128_f8f6f4 v[114:117], v[26:33], v[220:227], v[114:117], v188, v189 op_sel_hi:[0,0,0]
	v_mfma_scale_f32_16x16x128_f8f6f4 v[106:109], v[18:25], v[220:227], v[106:109], v188, v189 op_sel_hi:[0,0,0]
	v_lshl_add_u64 v[246:247], s[58:59], 0, v[166:167]
	v_mfma_scale_f32_16x16x128_f8f6f4 v[150:153], v[10:17], v[192:199], v[150:153], v188, v189 op_sel_hi:[0,0,0]
	v_mfma_scale_f32_16x16x128_f8f6f4 v[142:145], v[2:9], v[192:199], v[142:145], v188, v189 op_sel_hi:[0,0,0]
	v_lshl_add_u64 v[248:249], v[240:241], 0, s[10:11]
	v_mfma_scale_f32_16x16x128_f8f6f4 v[134:137], v[10:17], v[200:207], v[134:137], v188, v189 op_sel_hi:[0,0,0]
	v_mfma_scale_f32_16x16x128_f8f6f4 v[126:129], v[2:9], v[200:207], v[126:129], v188, v189 op_sel_hi:[0,0,0]
	v_lshl_add_u64 v[250:251], s[58:59], 0, v[164:165]
	v_mfma_scale_f32_16x16x128_f8f6f4 v[118:121], v[10:17], v[208:215], v[118:121], v188, v189 op_sel_hi:[0,0,0]
	v_mfma_scale_f32_16x16x128_f8f6f4 v[110:113], v[2:9], v[208:215], v[110:113], v188, v189 op_sel_hi:[0,0,0]
	v_mfma_scale_f32_16x16x128_f8f6f4 v[102:105], v[10:17], v[220:227], v[102:105], v188, v189 op_sel_hi:[0,0,0]
	v_mfma_scale_f32_16x16x128_f8f6f4 v[98:101], v[2:9], v[220:227], v[98:101], v188, v189 op_sel_hi:[0,0,0]
	s_barrier
	s_add_i32 s26, s70, s35
	s_mov_b32 m0, s26
	ds_read_b128 v[192:195], v187 offset:16384
	ds_read_b128 v[196:199], v187 offset:17408
	ds_read_b128 v[200:203], v187 offset:18432
	ds_read_b128 v[204:207], v187 offset:19456
	ds_read_b128 v[208:211], v187 offset:20480
	ds_read_b128 v[212:215], v187 offset:21504
	ds_read_b128 v[220:223], v187 offset:22528
	ds_read_b128 v[224:227], v187 offset:23552
	global_load_lds_dwordx4 v[240:241], off
	s_add_i32 m0, s26, 0x2000
	s_add_i32 s26, s71, s35
	global_load_lds_dwordx4 v[242:243], off
	s_mov_b32 m0, s26
	s_nop 0
	global_load_lds_dwordx4 v[244:245], off
	s_add_i32 m0, s26, 0x2000
	s_nop 0
	global_load_lds_dwordx4 v[248:249], off
	s_mov_b32 m0, s55
	s_nop 0
	global_load_lds_dwordx4 v[250:251], off
	s_mov_b32 m0, s63
	s_nop 0
	global_load_lds_dwordx4 v[246:247], off
	s_waitcnt vmcnt(8)
	s_waitcnt lgkmcnt(0)
	s_barrier
	s_waitcnt lgkmcnt(0)
	v_mfma_scale_f32_16x16x128_f8f6f4 v[94:97], v[26:33], v[192:199], v[94:97], v188, v189 op_sel_hi:[0,0,0]
	v_mfma_scale_f32_16x16x128_f8f6f4 v[90:93], v[18:25], v[192:199], v[90:93], v188, v189 op_sel_hi:[0,0,0]
	v_mfma_scale_f32_16x16x128_f8f6f4 v[82:85], v[26:33], v[200:207], v[82:85], v188, v189 op_sel_hi:[0,0,0]
	v_mfma_scale_f32_16x16x128_f8f6f4 v[74:77], v[18:25], v[200:207], v[74:77], v188, v189 op_sel_hi:[0,0,0]
	v_mfma_scale_f32_16x16x128_f8f6f4 v[66:69], v[26:33], v[208:215], v[66:69], v188, v189 op_sel_hi:[0,0,0]
	v_mfma_scale_f32_16x16x128_f8f6f4 v[58:61], v[18:25], v[208:215], v[58:61], v188, v189 op_sel_hi:[0,0,0]
	v_mfma_scale_f32_16x16x128_f8f6f4 v[50:53], v[26:33], v[220:227], v[50:53], v188, v189 op_sel_hi:[0,0,0]
	v_mfma_scale_f32_16x16x128_f8f6f4 v[42:45], v[18:25], v[220:227], v[42:45], v188, v189 op_sel_hi:[0,0,0]
	v_mfma_scale_f32_16x16x128_f8f6f4 v[86:89], v[10:17], v[192:199], v[86:89], v188, v189 op_sel_hi:[0,0,0]
	v_mfma_scale_f32_16x16x128_f8f6f4 v[78:81], v[2:9], v[192:199], v[78:81], v188, v189 op_sel_hi:[0,0,0]
	v_mfma_scale_f32_16x16x128_f8f6f4 v[70:73], v[10:17], v[200:207], v[70:73], v188, v189 op_sel_hi:[0,0,0]
	v_mfma_scale_f32_16x16x128_f8f6f4 v[62:65], v[2:9], v[200:207], v[62:65], v188, v189 op_sel_hi:[0,0,0]
	v_mfma_scale_f32_16x16x128_f8f6f4 v[54:57], v[10:17], v[208:215], v[54:57], v188, v189 op_sel_hi:[0,0,0]
	v_mfma_scale_f32_16x16x128_f8f6f4 v[46:49], v[2:9], v[208:215], v[46:49], v188, v189 op_sel_hi:[0,0,0]
	v_mfma_scale_f32_16x16x128_f8f6f4 v[38:41], v[10:17], v[220:227], v[38:41], v188, v189 op_sel_hi:[0,0,0]
	v_mfma_scale_f32_16x16x128_f8f6f4 v[34:37], v[2:9], v[220:227], v[34:37], v188, v189 op_sel_hi:[0,0,0]
	s_barrier
	s_add_i32 s60, 0, 0x18000
	s_add_i32 s61, 0, 0x1c000
	v_add_u32_e32 v14, s60, v183
	v_add_u32_e32 v30, s61, v183
	ds_read_b128 v[2:5], v14
	ds_read_b128 v[6:9], v14 offset:1024
	ds_read_b128 v[10:13], v14 offset:2048
	ds_read_b128 v[14:17], v14 offset:3072
	ds_read_b128 v[18:21], v30
	ds_read_b128 v[22:25], v30 offset:1024
	ds_read_b128 v[26:29], v30 offset:2048
	ds_read_b128 v[30:33], v30 offset:3072
	s_add_u32 s26, s58, 0x40000
	s_addc_u32 s27, s59, 0
	s_mov_b32 m0, s64
	v_lshl_add_u64 v[216:217], s[26:27], 0, v[164:165]
	ds_read_b128 v[192:195], v187 offset:32768
	ds_read_b128 v[196:199], v187 offset:33792
	ds_read_b128 v[200:203], v187 offset:34816
	ds_read_b128 v[204:207], v187 offset:35840
	ds_read_b128 v[208:211], v187 offset:36864
	ds_read_b128 v[212:215], v187 offset:37888
	ds_read_b128 v[220:223], v187 offset:38912
	ds_read_b128 v[224:227], v187 offset:39936
	global_load_lds_dwordx4 v[216:217], off
	v_lshl_add_u64 v[216:217], s[26:27], 0, v[166:167]
	s_mov_b32 m0, s65
	s_nop 0
	global_load_lds_dwordx4 v[216:217], off
	s_waitcnt vmcnt(8)
	s_waitcnt lgkmcnt(0)
	s_barrier
	s_waitcnt lgkmcnt(0)
	v_mfma_scale_f32_16x16x128_f8f6f4 v[158:161], v[2:9], v[192:199], v[158:161], v188, v189 op_sel_hi:[0,0,0]
	v_mfma_scale_f32_16x16x128_f8f6f4 v[154:157], v[10:17], v[192:199], v[154:157], v188, v189 op_sel_hi:[0,0,0]
	v_lshl_add_u64 v[242:243], v[240:241], 0, s[14:15]
	v_mfma_scale_f32_16x16x128_f8f6f4 v[146:149], v[2:9], v[200:207], v[146:149], v188, v189 op_sel_hi:[0,0,0]
	v_mfma_scale_f32_16x16x128_f8f6f4 v[138:141], v[10:17], v[200:207], v[138:141], v188, v189 op_sel_hi:[0,0,0]
	v_lshl_add_u64 v[244:245], v[240:241], 0, s[16:17]
	v_mfma_scale_f32_16x16x128_f8f6f4 v[130:133], v[2:9], v[208:215], v[130:133], v188, v189 op_sel_hi:[0,0,0]
	v_mfma_scale_f32_16x16x128_f8f6f4 v[122:125], v[10:17], v[208:215], v[122:125], v188, v189 op_sel_hi:[0,0,0]
	v_lshl_add_u64 v[248:249], v[240:241], 0, s[20:21]
	v_mfma_scale_f32_16x16x128_f8f6f4 v[114:117], v[2:9], v[220:227], v[114:117], v188, v189 op_sel_hi:[0,0,0]
	v_mfma_scale_f32_16x16x128_f8f6f4 v[106:109], v[10:17], v[220:227], v[106:109], v188, v189 op_sel_hi:[0,0,0]
	v_lshl_add_u64 v[240:241], v[240:241], 0, s[22:23]
	v_mfma_scale_f32_16x16x128_f8f6f4 v[150:153], v[18:25], v[192:199], v[150:153], v188, v189 op_sel_hi:[0,0,0]
	v_mfma_scale_f32_16x16x128_f8f6f4 v[142:145], v[26:33], v[192:199], v[142:145], v188, v189 op_sel_hi:[0,0,0]
	v_lshl_add_u64 v[250:251], v[250:251], 0, s[18:19]
	v_mfma_scale_f32_16x16x128_f8f6f4 v[134:137], v[18:25], v[200:207], v[134:137], v188, v189 op_sel_hi:[0,0,0]
	v_mfma_scale_f32_16x16x128_f8f6f4 v[126:129], v[26:33], v[200:207], v[126:129], v188, v189 op_sel_hi:[0,0,0]
	v_lshl_add_u64 v[246:247], v[246:247], 0, s[18:19]
	v_mfma_scale_f32_16x16x128_f8f6f4 v[118:121], v[18:25], v[208:215], v[118:121], v188, v189 op_sel_hi:[0,0,0]
	v_mfma_scale_f32_16x16x128_f8f6f4 v[110:113], v[26:33], v[208:215], v[110:113], v188, v189 op_sel_hi:[0,0,0]
	v_mfma_scale_f32_16x16x128_f8f6f4 v[102:105], v[18:25], v[220:227], v[102:105], v188, v189 op_sel_hi:[0,0,0]
	v_mfma_scale_f32_16x16x128_f8f6f4 v[98:101], v[26:33], v[220:227], v[98:101], v188, v189 op_sel_hi:[0,0,0]
	s_barrier
	s_add_i32 s26, s60, s35
	s_mov_b32 m0, s26
	ds_read_b128 v[192:195], v187 offset:49152
	ds_read_b128 v[196:199], v187 offset:50176
	ds_read_b128 v[200:203], v187 offset:51200
	ds_read_b128 v[204:207], v187 offset:52224
	ds_read_b128 v[208:211], v187 offset:53248
	ds_read_b128 v[212:215], v187 offset:54272
	ds_read_b128 v[220:223], v187 offset:55296
	ds_read_b128 v[224:227], v187 offset:56320
	global_load_lds_dwordx4 v[242:243], off
	s_add_i32 m0, s26, 0x2000
	s_add_i32 s26, s61, s35
	global_load_lds_dwordx4 v[244:245], off
	s_mov_b32 m0, s26
	s_nop 0
	global_load_lds_dwordx4 v[248:249], off
	s_add_i32 m0, s26, 0x2000
	s_nop 0
	global_load_lds_dwordx4 v[240:241], off
	s_mov_b32 m0, s67
	s_nop 0
	global_load_lds_dwordx4 v[250:251], off
	s_mov_b32 m0, s68
	s_nop 0
	global_load_lds_dwordx4 v[246:247], off
	s_waitcnt vmcnt(8)
	s_waitcnt lgkmcnt(0)
	s_barrier
	s_waitcnt lgkmcnt(0)
	v_mfma_scale_f32_16x16x128_f8f6f4 v[94:97], v[2:9], v[192:199], v[94:97], v188, v189 op_sel_hi:[0,0,0]
	v_mfma_scale_f32_16x16x128_f8f6f4 v[90:93], v[10:17], v[192:199], v[90:93], v188, v189 op_sel_hi:[0,0,0]
	v_mfma_scale_f32_16x16x128_f8f6f4 v[82:85], v[2:9], v[200:207], v[82:85], v188, v189 op_sel_hi:[0,0,0]
	v_mfma_scale_f32_16x16x128_f8f6f4 v[74:77], v[10:17], v[200:207], v[74:77], v188, v189 op_sel_hi:[0,0,0]
	v_mfma_scale_f32_16x16x128_f8f6f4 v[66:69], v[2:9], v[208:215], v[66:69], v188, v189 op_sel_hi:[0,0,0]
	v_mfma_scale_f32_16x16x128_f8f6f4 v[58:61], v[10:17], v[208:215], v[58:61], v188, v189 op_sel_hi:[0,0,0]
	v_mfma_scale_f32_16x16x128_f8f6f4 v[50:53], v[2:9], v[220:227], v[50:53], v188, v189 op_sel_hi:[0,0,0]
	v_mfma_scale_f32_16x16x128_f8f6f4 v[42:45], v[10:17], v[220:227], v[42:45], v188, v189 op_sel_hi:[0,0,0]
	v_mfma_scale_f32_16x16x128_f8f6f4 v[86:89], v[18:25], v[192:199], v[86:89], v188, v189 op_sel_hi:[0,0,0]
	v_mfma_scale_f32_16x16x128_f8f6f4 v[78:81], v[26:33], v[192:199], v[78:81], v188, v189 op_sel_hi:[0,0,0]
	v_mfma_scale_f32_16x16x128_f8f6f4 v[70:73], v[18:25], v[200:207], v[70:73], v188, v189 op_sel_hi:[0,0,0]
	v_mfma_scale_f32_16x16x128_f8f6f4 v[62:65], v[26:33], v[200:207], v[62:65], v188, v189 op_sel_hi:[0,0,0]
	v_mfma_scale_f32_16x16x128_f8f6f4 v[54:57], v[18:25], v[208:215], v[54:57], v188, v189 op_sel_hi:[0,0,0]
	v_mfma_scale_f32_16x16x128_f8f6f4 v[46:49], v[26:33], v[208:215], v[46:49], v188, v189 op_sel_hi:[0,0,0]
	v_mfma_scale_f32_16x16x128_f8f6f4 v[38:41], v[18:25], v[220:227], v[38:41], v188, v189 op_sel_hi:[0,0,0]
	v_mfma_scale_f32_16x16x128_f8f6f4 v[34:37], v[26:33], v[220:227], v[34:37], v188, v189 op_sel_hi:[0,0,0]
	s_barrier
	s_add_i32 s80, s80, 2
	s_add_u32 s74, s74, 0x10000
	s_addc_u32 s75, s75, 0
	s_add_u32 s56, s56, 0x100
	s_addc_u32 s57, s57, 0
	s_cmp_gt_u32 s80, 13
	s_cbranch_scc0 .LBB0_985
	s_and_b64 vcc, exec, s[24:25]
	s_cbranch_vccz .LBB0_988
	s_barrier

.LBB0_1192:
	ds_read_b128 v[66:69], v199
	ds_read_b128 v[70:73], v199 offset:1024
	ds_read_b128 v[82:85], v199 offset:2048
	ds_read_b128 v[86:89], v199 offset:3072
	ds_read_b128 v[146:149], v200
	ds_read_b128 v[150:153], v200 offset:1024
	ds_read_b128 v[154:157], v200 offset:2048
	ds_read_b128 v[158:161], v200 offset:3072
	s_add_u32 s26, s56, 0xfffc0080
	s_addc_u32 s27, s57, -1
	s_cmp_eq_u32 s73, 12
	s_cselect_b32 s59, s45, s27
	s_cselect_b32 s58, s69, s26
	s_cselect_b32 s27, s41, s72
	s_cselect_b32 s26, s70, s71
	v_lshl_add_u64 v[214:215], s[56:57], 0, v[176:177]
	s_add_i32 m0, s55, 0xc000
	ds_read_b128 v[162:165], v201
	ds_read_b128 v[166:169], v201 offset:1024
	ds_read_b128 v[184:187], v201 offset:2048
	ds_read_b128 v[188:191], v201 offset:3072
	ds_read_b128 v[192:195], v201 offset:4096
	ds_read_b128 v[202:205], v201 offset:5120
	ds_read_b128 v[206:209], v201 offset:6144
	ds_read_b128 v[210:213], v201 offset:7168
	global_load_lds_dwordx4 v[214:215], off
	v_lshl_add_u64 v[214:215], s[56:57], 0, v[178:179]
	s_add_i32 m0, s55, 0xe000
	s_nop 0
	global_load_lds_dwordx4 v[214:215], off
	s_waitcnt vmcnt(8)
	s_waitcnt lgkmcnt(0)
	s_barrier
	s_waitcnt lgkmcnt(0)
	v_mfma_f32_16x16x32_bf16 v[142:145], v[66:69], v[162:165], v[142:145]
	v_mfma_f32_16x16x32_bf16 v[138:141], v[82:85], v[162:165], v[138:141]
	v_lshl_add_u64 v[240:241], s[26:27], 0, v[170:171]
	v_mfma_f32_16x16x32_bf16 v[126:129], v[66:69], v[184:187], v[126:129]
	v_mfma_f32_16x16x32_bf16 v[122:125], v[82:85], v[184:187], v[122:125]
	v_lshl_add_u64 v[242:243], v[240:241], 0, s[6:7]
	v_mfma_f32_16x16x32_bf16 v[110:113], v[66:69], v[192:195], v[110:113]
	v_mfma_f32_16x16x32_bf16 v[106:109], v[82:85], v[192:195], v[106:109]
	v_lshl_add_u64 v[244:245], v[240:241], 0, s[10:11]
	v_mfma_f32_16x16x32_bf16 v[94:97], v[66:69], v[206:209], v[94:97]
	v_mfma_f32_16x16x32_bf16 v[90:93], v[82:85], v[206:209], v[90:93]
	v_lshl_add_u64 v[246:247], s[58:59], 0, v[174:175]
	v_mfma_f32_16x16x32_bf16 v[142:145], v[70:73], v[166:169], v[142:145]
	v_mfma_f32_16x16x32_bf16 v[138:141], v[86:89], v[166:169], v[138:141]
	v_lshl_add_u64 v[248:249], v[240:241], 0, s[12:13]
	v_mfma_f32_16x16x32_bf16 v[126:129], v[70:73], v[188:191], v[126:129]
	v_mfma_f32_16x16x32_bf16 v[122:125], v[86:89], v[188:191], v[122:125]
	v_lshl_add_u64 v[250:251], s[58:59], 0, v[172:173]
	v_mfma_f32_16x16x32_bf16 v[110:113], v[70:73], v[202:205], v[110:113]
	v_mfma_f32_16x16x32_bf16 v[106:109], v[86:89], v[202:205], v[106:109]
	v_mfma_f32_16x16x32_bf16 v[94:97], v[70:73], v[210:213], v[94:97]
	v_mfma_f32_16x16x32_bf16 v[90:93], v[86:89], v[210:213], v[90:93]
	v_mfma_f32_16x16x32_bf16 v[134:137], v[146:149], v[162:165], v[134:137]
	v_mfma_f32_16x16x32_bf16 v[130:133], v[154:157], v[162:165], v[130:133]
	v_mfma_f32_16x16x32_bf16 v[118:121], v[146:149], v[184:187], v[118:121]
	v_mfma_f32_16x16x32_bf16 v[114:117], v[154:157], v[184:187], v[114:117]
	v_mfma_f32_16x16x32_bf16 v[102:105], v[146:149], v[192:195], v[102:105]
	v_mfma_f32_16x16x32_bf16 v[98:101], v[154:157], v[192:195], v[98:101]
	v_mfma_f32_16x16x32_bf16 v[78:81], v[146:149], v[206:209], v[78:81]
	v_mfma_f32_16x16x32_bf16 v[74:77], v[154:157], v[206:209], v[74:77]
	v_mfma_f32_16x16x32_bf16 v[134:137], v[150:153], v[166:169], v[134:137]
	v_mfma_f32_16x16x32_bf16 v[130:133], v[158:161], v[166:169], v[130:133]
	v_mfma_f32_16x16x32_bf16 v[118:121], v[150:153], v[188:191], v[118:121]
	v_mfma_f32_16x16x32_bf16 v[114:117], v[158:161], v[188:191], v[114:117]
	v_mfma_f32_16x16x32_bf16 v[102:105], v[150:153], v[202:205], v[102:105]
	v_mfma_f32_16x16x32_bf16 v[98:101], v[158:161], v[202:205], v[98:101]
	v_mfma_f32_16x16x32_bf16 v[78:81], v[150:153], v[210:213], v[78:81]
	v_mfma_f32_16x16x32_bf16 v[74:77], v[158:161], v[210:213], v[74:77]
	s_barrier
	s_add_i32 s26, s67, s35
	s_mov_b32 m0, s26
	ds_read_b128 v[162:165], v201 offset:16384
	ds_read_b128 v[166:169], v201 offset:17408
	ds_read_b128 v[184:187], v201 offset:18432
	ds_read_b128 v[188:191], v201 offset:19456
	ds_read_b128 v[192:195], v201 offset:20480
	ds_read_b128 v[202:205], v201 offset:21504
	ds_read_b128 v[206:209], v201 offset:22528
	ds_read_b128 v[210:213], v201 offset:23552
	global_load_lds_dwordx4 v[240:241], off
	s_add_i32 m0, s26, 0x2000
	s_add_i32 s26, s68, s35
	global_load_lds_dwordx4 v[242:243], off
	s_mov_b32 m0, s26
	s_nop 0
	global_load_lds_dwordx4 v[244:245], off
	s_add_i32 m0, s26, 0x2000
	s_nop 0
	global_load_lds_dwordx4 v[248:249], off
	s_mov_b32 m0, s55
	s_nop 0
	global_load_lds_dwordx4 v[250:251], off
	s_mov_b32 m0, s60
	s_nop 0
	global_load_lds_dwordx4 v[246:247], off
	s_waitcnt vmcnt(8)
	s_waitcnt lgkmcnt(0)
	s_barrier
	s_waitcnt lgkmcnt(0)
	v_mfma_f32_16x16x32_bf16 v[62:65], v[66:69], v[162:165], v[62:65]
	v_mfma_f32_16x16x32_bf16 v[58:61], v[82:85], v[162:165], v[58:61]
	v_mfma_f32_16x16x32_bf16 v[46:49], v[66:69], v[184:187], v[46:49]
	v_mfma_f32_16x16x32_bf16 v[42:45], v[82:85], v[184:187], v[42:45]
	v_mfma_f32_16x16x32_bf16 v[30:33], v[66:69], v[192:195], v[30:33]
	v_mfma_f32_16x16x32_bf16 v[26:29], v[82:85], v[192:195], v[26:29]
	v_mfma_f32_16x16x32_bf16 v[14:17], v[66:69], v[206:209], v[14:17]
	v_mfma_f32_16x16x32_bf16 v[10:13], v[82:85], v[206:209], v[10:13]
	v_mfma_f32_16x16x32_bf16 v[62:65], v[70:73], v[166:169], v[62:65]
	v_mfma_f32_16x16x32_bf16 v[58:61], v[86:89], v[166:169], v[58:61]
	v_mfma_f32_16x16x32_bf16 v[46:49], v[70:73], v[188:191], v[46:49]
	v_mfma_f32_16x16x32_bf16 v[42:45], v[86:89], v[188:191], v[42:45]
	v_mfma_f32_16x16x32_bf16 v[30:33], v[70:73], v[202:205], v[30:33]
	v_mfma_f32_16x16x32_bf16 v[26:29], v[86:89], v[202:205], v[26:29]
	v_mfma_f32_16x16x32_bf16 v[14:17], v[70:73], v[210:213], v[14:17]
	v_mfma_f32_16x16x32_bf16 v[10:13], v[86:89], v[210:213], v[10:13]
	v_mfma_f32_16x16x32_bf16 v[54:57], v[146:149], v[162:165], v[54:57]
	v_mfma_f32_16x16x32_bf16 v[50:53], v[154:157], v[162:165], v[50:53]
	v_mfma_f32_16x16x32_bf16 v[38:41], v[146:149], v[184:187], v[38:41]
	v_mfma_f32_16x16x32_bf16 v[34:37], v[154:157], v[184:187], v[34:37]
	v_mfma_f32_16x16x32_bf16 v[22:25], v[146:149], v[192:195], v[22:25]
	v_mfma_f32_16x16x32_bf16 v[18:21], v[154:157], v[192:195], v[18:21]
	v_mfma_f32_16x16x32_bf16 v[6:9], v[146:149], v[206:209], v[6:9]
	v_mfma_f32_16x16x32_bf16 v[2:5], v[154:157], v[206:209], v[2:5]
	v_mfma_f32_16x16x32_bf16 v[54:57], v[150:153], v[166:169], v[54:57]
	v_mfma_f32_16x16x32_bf16 v[50:53], v[158:161], v[166:169], v[50:53]
	v_mfma_f32_16x16x32_bf16 v[38:41], v[150:153], v[188:191], v[38:41]
	v_mfma_f32_16x16x32_bf16 v[34:37], v[158:161], v[188:191], v[34:37]
	v_mfma_f32_16x16x32_bf16 v[22:25], v[150:153], v[202:205], v[22:25]
	v_mfma_f32_16x16x32_bf16 v[18:21], v[158:161], v[202:205], v[18:21]
	v_mfma_f32_16x16x32_bf16 v[6:9], v[150:153], v[210:213], v[6:9]
	v_mfma_f32_16x16x32_bf16 v[2:5], v[158:161], v[210:213], v[2:5]
	s_barrier
	s_add_i32 s74, 0, 0x18000
	s_add_i32 s75, 0, 0x1c000
	v_add_u32_e32 v86, s74, v197
	v_add_u32_e32 v158, s75, v197
	ds_read_b128 v[66:69], v86
	ds_read_b128 v[70:73], v86 offset:1024
	ds_read_b128 v[82:85], v86 offset:2048
	ds_read_b128 v[86:89], v86 offset:3072
	ds_read_b128 v[146:149], v158
	ds_read_b128 v[150:153], v158 offset:1024
	ds_read_b128 v[154:157], v158 offset:2048
	ds_read_b128 v[158:161], v158 offset:3072
	s_add_u32 s26, s58, 0x40000
	s_addc_u32 s27, s59, 0
	s_mov_b32 m0, s61
	v_lshl_add_u64 v[222:223], s[26:27], 0, v[172:173]
	ds_read_b128 v[162:165], v201 offset:32768
	ds_read_b128 v[166:169], v201 offset:33792
	ds_read_b128 v[184:187], v201 offset:34816
	ds_read_b128 v[188:191], v201 offset:35840
	ds_read_b128 v[192:195], v201 offset:36864
	ds_read_b128 v[202:205], v201 offset:37888
	ds_read_b128 v[206:209], v201 offset:38912
	ds_read_b128 v[210:213], v201 offset:39936
	global_load_lds_dwordx4 v[222:223], off
	v_lshl_add_u64 v[222:223], s[26:27], 0, v[174:175]
	s_mov_b32 m0, s62
	s_nop 0
	global_load_lds_dwordx4 v[222:223], off
	s_waitcnt vmcnt(8)
	s_waitcnt lgkmcnt(0)
	s_barrier
	s_waitcnt lgkmcnt(0)
	v_mfma_f32_16x16x32_bf16 v[142:145], v[66:69], v[162:165], v[142:145]
	v_mfma_f32_16x16x32_bf16 v[138:141], v[82:85], v[162:165], v[138:141]
	v_lshl_add_u64 v[242:243], v[240:241], 0, s[16:17]
	v_mfma_f32_16x16x32_bf16 v[126:129], v[66:69], v[184:187], v[126:129]
	v_mfma_f32_16x16x32_bf16 v[122:125], v[82:85], v[184:187], v[122:125]
	v_lshl_add_u64 v[244:245], v[240:241], 0, s[18:19]
	v_mfma_f32_16x16x32_bf16 v[110:113], v[66:69], v[192:195], v[110:113]
	v_mfma_f32_16x16x32_bf16 v[106:109], v[82:85], v[192:195], v[106:109]
	v_lshl_add_u64 v[248:249], v[240:241], 0, s[22:23]
	v_mfma_f32_16x16x32_bf16 v[94:97], v[66:69], v[206:209], v[94:97]
	v_mfma_f32_16x16x32_bf16 v[90:93], v[82:85], v[206:209], v[90:93]
	v_lshl_add_u64 v[240:241], v[240:241], 0, s[24:25]
	v_mfma_f32_16x16x32_bf16 v[142:145], v[70:73], v[166:169], v[142:145]
	v_mfma_f32_16x16x32_bf16 v[138:141], v[86:89], v[166:169], v[138:141]
	v_lshl_add_u64 v[250:251], v[250:251], 0, s[20:21]
	v_mfma_f32_16x16x32_bf16 v[126:129], v[70:73], v[188:191], v[126:129]
	v_mfma_f32_16x16x32_bf16 v[122:125], v[86:89], v[188:191], v[122:125]
	v_lshl_add_u64 v[246:247], v[246:247], 0, s[20:21]
	v_mfma_f32_16x16x32_bf16 v[110:113], v[70:73], v[202:205], v[110:113]
	v_mfma_f32_16x16x32_bf16 v[106:109], v[86:89], v[202:205], v[106:109]
	v_mfma_f32_16x16x32_bf16 v[94:97], v[70:73], v[210:213], v[94:97]
	v_mfma_f32_16x16x32_bf16 v[90:93], v[86:89], v[210:213], v[90:93]
	v_mfma_f32_16x16x32_bf16 v[134:137], v[146:149], v[162:165], v[134:137]
	v_mfma_f32_16x16x32_bf16 v[130:133], v[154:157], v[162:165], v[130:133]
	v_mfma_f32_16x16x32_bf16 v[118:121], v[146:149], v[184:187], v[118:121]
	v_mfma_f32_16x16x32_bf16 v[114:117], v[154:157], v[184:187], v[114:117]
	v_mfma_f32_16x16x32_bf16 v[102:105], v[146:149], v[192:195], v[102:105]
	v_mfma_f32_16x16x32_bf16 v[98:101], v[154:157], v[192:195], v[98:101]
	v_mfma_f32_16x16x32_bf16 v[78:81], v[146:149], v[206:209], v[78:81]
	v_mfma_f32_16x16x32_bf16 v[74:77], v[154:157], v[206:209], v[74:77]
	v_mfma_f32_16x16x32_bf16 v[134:137], v[150:153], v[166:169], v[134:137]
	v_mfma_f32_16x16x32_bf16 v[130:133], v[158:161], v[166:169], v[130:133]
	v_mfma_f32_16x16x32_bf16 v[118:121], v[150:153], v[188:191], v[118:121]
	v_mfma_f32_16x16x32_bf16 v[114:117], v[158:161], v[188:191], v[114:117]
	v_mfma_f32_16x16x32_bf16 v[102:105], v[150:153], v[202:205], v[102:105]
	v_mfma_f32_16x16x32_bf16 v[98:101], v[158:161], v[202:205], v[98:101]
	v_mfma_f32_16x16x32_bf16 v[78:81], v[150:153], v[210:213], v[78:81]
	v_mfma_f32_16x16x32_bf16 v[74:77], v[158:161], v[210:213], v[74:77]
	s_barrier
	s_add_i32 s26, s74, s35
	s_mov_b32 m0, s26
	ds_read_b128 v[162:165], v201 offset:49152
	ds_read_b128 v[166:169], v201 offset:50176
	ds_read_b128 v[184:187], v201 offset:51200
	ds_read_b128 v[188:191], v201 offset:52224
	ds_read_b128 v[192:195], v201 offset:53248
	ds_read_b128 v[202:205], v201 offset:54272
	ds_read_b128 v[206:209], v201 offset:55296
	ds_read_b128 v[210:213], v201 offset:56320
	global_load_lds_dwordx4 v[242:243], off
	s_add_i32 m0, s26, 0x2000
	s_add_i32 s26, s75, s35
	global_load_lds_dwordx4 v[244:245], off
	s_mov_b32 m0, s26
	s_nop 0
	global_load_lds_dwordx4 v[248:249], off
	s_add_i32 m0, s26, 0x2000
	s_nop 0
	global_load_lds_dwordx4 v[240:241], off
	s_mov_b32 m0, s64
	s_nop 0
	global_load_lds_dwordx4 v[250:251], off
	s_mov_b32 m0, s65
	s_nop 0
	global_load_lds_dwordx4 v[246:247], off
	s_waitcnt vmcnt(8)
	s_waitcnt lgkmcnt(0)
	s_barrier
	s_waitcnt lgkmcnt(0)
	v_mfma_f32_16x16x32_bf16 v[62:65], v[66:69], v[162:165], v[62:65]
	v_mfma_f32_16x16x32_bf16 v[58:61], v[82:85], v[162:165], v[58:61]
	v_mfma_f32_16x16x32_bf16 v[46:49], v[66:69], v[184:187], v[46:49]
	v_mfma_f32_16x16x32_bf16 v[42:45], v[82:85], v[184:187], v[42:45]
	v_mfma_f32_16x16x32_bf16 v[30:33], v[66:69], v[192:195], v[30:33]
	v_mfma_f32_16x16x32_bf16 v[26:29], v[82:85], v[192:195], v[26:29]
	v_mfma_f32_16x16x32_bf16 v[14:17], v[66:69], v[206:209], v[14:17]
	v_mfma_f32_16x16x32_bf16 v[10:13], v[82:85], v[206:209], v[10:13]
	v_mfma_f32_16x16x32_bf16 v[62:65], v[70:73], v[166:169], v[62:65]
	v_mfma_f32_16x16x32_bf16 v[58:61], v[86:89], v[166:169], v[58:61]
	v_mfma_f32_16x16x32_bf16 v[46:49], v[70:73], v[188:191], v[46:49]
	v_mfma_f32_16x16x32_bf16 v[42:45], v[86:89], v[188:191], v[42:45]
	v_mfma_f32_16x16x32_bf16 v[30:33], v[70:73], v[202:205], v[30:33]
	v_mfma_f32_16x16x32_bf16 v[26:29], v[86:89], v[202:205], v[26:29]
	v_mfma_f32_16x16x32_bf16 v[14:17], v[70:73], v[210:213], v[14:17]
	v_mfma_f32_16x16x32_bf16 v[10:13], v[86:89], v[210:213], v[10:13]
	v_mfma_f32_16x16x32_bf16 v[54:57], v[146:149], v[162:165], v[54:57]
	v_mfma_f32_16x16x32_bf16 v[50:53], v[154:157], v[162:165], v[50:53]
	v_mfma_f32_16x16x32_bf16 v[38:41], v[146:149], v[184:187], v[38:41]
	v_mfma_f32_16x16x32_bf16 v[34:37], v[154:157], v[184:187], v[34:37]
	v_mfma_f32_16x16x32_bf16 v[22:25], v[146:149], v[192:195], v[22:25]
	v_mfma_f32_16x16x32_bf16 v[18:21], v[154:157], v[192:195], v[18:21]
	v_mfma_f32_16x16x32_bf16 v[6:9], v[146:149], v[206:209], v[6:9]
	v_mfma_f32_16x16x32_bf16 v[2:5], v[154:157], v[206:209], v[2:5]
	v_mfma_f32_16x16x32_bf16 v[54:57], v[150:153], v[166:169], v[54:57]
	v_mfma_f32_16x16x32_bf16 v[50:53], v[158:161], v[166:169], v[50:53]
	v_mfma_f32_16x16x32_bf16 v[38:41], v[150:153], v[188:191], v[38:41]
	v_mfma_f32_16x16x32_bf16 v[34:37], v[158:161], v[188:191], v[34:37]
	v_mfma_f32_16x16x32_bf16 v[22:25], v[150:153], v[202:205], v[22:25]
	v_mfma_f32_16x16x32_bf16 v[18:21], v[158:161], v[202:205], v[18:21]
	v_mfma_f32_16x16x32_bf16 v[6:9], v[150:153], v[210:213], v[6:9]
	v_mfma_f32_16x16x32_bf16 v[2:5], v[158:161], v[210:213], v[2:5]
	s_barrier
	s_add_i32 s73, s73, 2
	s_add_u32 s71, s71, 0x10000
	s_addc_u32 s72, s72, 0
	s_add_u32 s56, s56, 0x100
	s_addc_u32 s57, s57, 0
	s_cmp_gt_u32 s73, 13
	s_cbranch_scc0 .LBB0_1192
	s_and_b64 vcc, exec, s[36:37]
	s_cbranch_vccz .LBB0_1195
	s_barrier

.LBB0_1271:
	ds_read_b128 v[144:147], v158
	ds_read_b128 v[148:151], v158 offset:1024
	ds_read_b128 v[152:155], v158 offset:2048
	ds_read_b128 v[162:165], v158 offset:3072
	ds_read_b128 v[166:169], v159
	ds_read_b128 v[170:173], v159 offset:1024
	ds_read_b128 v[174:177], v159 offset:2048
	ds_read_b128 v[178:181], v159 offset:3072
	s_add_u32 s26, s58, 0xfff80080
	s_addc_u32 s27, s59, -1
	s_cmp_eq_u32 s80, 28
	s_cselect_b32 s61, s51, s27
	s_cselect_b32 s60, s57, s26
	s_cselect_b32 s27, s45, s75
	s_cselect_b32 s26, s73, s74
	v_lshl_add_u64 v[214:215], s[58:59], 0, v[136:137]
	s_add_i32 m0, s63, 0xc000
	ds_read_b128 v[182:185], v160
	ds_read_b128 v[186:189], v160 offset:1024
	ds_read_b128 v[190:193], v160 offset:2048
	ds_read_b128 v[194:197], v160 offset:3072
	ds_read_b128 v[198:201], v160 offset:4096
	ds_read_b128 v[202:205], v160 offset:5120
	ds_read_b128 v[206:209], v160 offset:6144
	ds_read_b128 v[210:213], v160 offset:7168
	global_load_lds_dwordx4 v[214:215], off
	v_lshl_add_u64 v[214:215], s[58:59], 0, v[138:139]
	s_add_i32 m0, s63, 0xe000
	s_nop 0
	global_load_lds_dwordx4 v[214:215], off
	s_waitcnt vmcnt(8)
	s_waitcnt lgkmcnt(0)
	s_barrier
	s_waitcnt lgkmcnt(0)
	v_mfma_f32_16x16x32_bf16 v[126:129], v[144:147], v[182:185], v[126:129]
	v_mfma_f32_16x16x32_bf16 v[122:125], v[152:155], v[182:185], v[122:125]
	v_lshl_add_u64 v[240:241], s[26:27], 0, v[130:131]
	v_mfma_f32_16x16x32_bf16 v[118:121], v[144:147], v[190:193], v[118:121]
	v_mfma_f32_16x16x32_bf16 v[114:117], v[152:155], v[190:193], v[114:117]
	v_lshl_add_u64 v[242:243], v[240:241], 0, s[6:7]
	v_mfma_f32_16x16x32_bf16 v[106:109], v[144:147], v[198:201], v[106:109]
	v_mfma_f32_16x16x32_bf16 v[98:101], v[152:155], v[198:201], v[98:101]
	v_lshl_add_u64 v[244:245], v[240:241], 0, s[8:9]
	v_mfma_f32_16x16x32_bf16 v[90:93], v[144:147], v[206:209], v[90:93]
	v_mfma_f32_16x16x32_bf16 v[82:85], v[152:155], v[206:209], v[82:85]
	v_lshl_add_u64 v[246:247], s[60:61], 0, v[134:135]
	v_mfma_f32_16x16x32_bf16 v[126:129], v[148:151], v[186:189], v[126:129]
	v_mfma_f32_16x16x32_bf16 v[122:125], v[162:165], v[186:189], v[122:125]
	v_lshl_add_u64 v[248:249], v[240:241], 0, s[10:11]
	v_mfma_f32_16x16x32_bf16 v[118:121], v[148:151], v[194:197], v[118:121]
	v_mfma_f32_16x16x32_bf16 v[114:117], v[162:165], v[194:197], v[114:117]
	v_lshl_add_u64 v[250:251], s[60:61], 0, v[132:133]
	v_mfma_f32_16x16x32_bf16 v[106:109], v[148:151], v[202:205], v[106:109]
	v_mfma_f32_16x16x32_bf16 v[98:101], v[162:165], v[202:205], v[98:101]
	v_mfma_f32_16x16x32_bf16 v[90:93], v[148:151], v[210:213], v[90:93]
	v_mfma_f32_16x16x32_bf16 v[82:85], v[162:165], v[210:213], v[82:85]
	v_mfma_f32_16x16x32_bf16 v[110:113], v[166:169], v[182:185], v[110:113]
	v_mfma_f32_16x16x32_bf16 v[102:105], v[174:177], v[182:185], v[102:105]
	v_mfma_f32_16x16x32_bf16 v[94:97], v[166:169], v[190:193], v[94:97]
	v_mfma_f32_16x16x32_bf16 v[86:89], v[174:177], v[190:193], v[86:89]
	v_mfma_f32_16x16x32_bf16 v[78:81], v[166:169], v[198:201], v[78:81]
	v_mfma_f32_16x16x32_bf16 v[74:77], v[174:177], v[198:201], v[74:77]
	v_mfma_f32_16x16x32_bf16 v[70:73], v[166:169], v[206:209], v[70:73]
	v_mfma_f32_16x16x32_bf16 v[66:69], v[174:177], v[206:209], v[66:69]
	v_mfma_f32_16x16x32_bf16 v[110:113], v[170:173], v[186:189], v[110:113]
	v_mfma_f32_16x16x32_bf16 v[102:105], v[178:181], v[186:189], v[102:105]
	v_mfma_f32_16x16x32_bf16 v[94:97], v[170:173], v[194:197], v[94:97]
	v_mfma_f32_16x16x32_bf16 v[86:89], v[178:181], v[194:197], v[86:89]
	v_mfma_f32_16x16x32_bf16 v[78:81], v[170:173], v[202:205], v[78:81]
	v_mfma_f32_16x16x32_bf16 v[74:77], v[178:181], v[202:205], v[74:77]
	v_mfma_f32_16x16x32_bf16 v[70:73], v[170:173], v[210:213], v[70:73]
	v_mfma_f32_16x16x32_bf16 v[66:69], v[178:181], v[210:213], v[66:69]
	s_barrier
	s_add_i32 s26, s71, s35
	s_mov_b32 m0, s26
	ds_read_b128 v[182:185], v160 offset:16384
	ds_read_b128 v[186:189], v160 offset:17408
	ds_read_b128 v[190:193], v160 offset:18432
	ds_read_b128 v[194:197], v160 offset:19456
	ds_read_b128 v[198:201], v160 offset:20480
	ds_read_b128 v[202:205], v160 offset:21504
	ds_read_b128 v[206:209], v160 offset:22528
	ds_read_b128 v[210:213], v160 offset:23552
	global_load_lds_dwordx4 v[240:241], off
	s_add_i32 m0, s26, 0x2000
	s_add_i32 s26, s72, s35
	global_load_lds_dwordx4 v[242:243], off
	s_mov_b32 m0, s26
	s_nop 0
	global_load_lds_dwordx4 v[244:245], off
	s_add_i32 m0, s26, 0x2000
	s_nop 0
	global_load_lds_dwordx4 v[248:249], off
	s_mov_b32 m0, s63
	s_nop 0
	global_load_lds_dwordx4 v[250:251], off
	s_mov_b32 m0, s64
	s_nop 0
	global_load_lds_dwordx4 v[246:247], off
	s_waitcnt vmcnt(8)
	s_waitcnt lgkmcnt(0)
	s_barrier
	s_waitcnt lgkmcnt(0)
	v_mfma_f32_16x16x32_bf16 v[62:65], v[144:147], v[182:185], v[62:65]
	v_mfma_f32_16x16x32_bf16 v[58:61], v[152:155], v[182:185], v[58:61]
	v_mfma_f32_16x16x32_bf16 v[54:57], v[144:147], v[190:193], v[54:57]
	v_mfma_f32_16x16x32_bf16 v[46:49], v[152:155], v[190:193], v[46:49]
	v_mfma_f32_16x16x32_bf16 v[38:41], v[144:147], v[198:201], v[38:41]
	v_mfma_f32_16x16x32_bf16 v[30:33], v[152:155], v[198:201], v[30:33]
	v_mfma_f32_16x16x32_bf16 v[22:25], v[144:147], v[206:209], v[22:25]
	v_mfma_f32_16x16x32_bf16 v[14:17], v[152:155], v[206:209], v[14:17]
	v_mfma_f32_16x16x32_bf16 v[62:65], v[148:151], v[186:189], v[62:65]
	v_mfma_f32_16x16x32_bf16 v[58:61], v[162:165], v[186:189], v[58:61]
	v_mfma_f32_16x16x32_bf16 v[54:57], v[148:151], v[194:197], v[54:57]
	v_mfma_f32_16x16x32_bf16 v[46:49], v[162:165], v[194:197], v[46:49]
	v_mfma_f32_16x16x32_bf16 v[38:41], v[148:151], v[202:205], v[38:41]
	v_mfma_f32_16x16x32_bf16 v[30:33], v[162:165], v[202:205], v[30:33]
	v_mfma_f32_16x16x32_bf16 v[22:25], v[148:151], v[210:213], v[22:25]
	v_mfma_f32_16x16x32_bf16 v[14:17], v[162:165], v[210:213], v[14:17]
	v_mfma_f32_16x16x32_bf16 v[50:53], v[166:169], v[182:185], v[50:53]
	v_mfma_f32_16x16x32_bf16 v[42:45], v[174:177], v[182:185], v[42:45]
	v_mfma_f32_16x16x32_bf16 v[34:37], v[166:169], v[190:193], v[34:37]
	v_mfma_f32_16x16x32_bf16 v[26:29], v[174:177], v[190:193], v[26:29]
	v_mfma_f32_16x16x32_bf16 v[18:21], v[166:169], v[198:201], v[18:21]
	v_mfma_f32_16x16x32_bf16 v[10:13], v[174:177], v[198:201], v[10:13]
	v_mfma_f32_16x16x32_bf16 v[6:9], v[166:169], v[206:209], v[6:9]
	v_mfma_f32_16x16x32_bf16 v[2:5], v[174:177], v[206:209], v[2:5]
	v_mfma_f32_16x16x32_bf16 v[50:53], v[170:173], v[186:189], v[50:53]
	v_mfma_f32_16x16x32_bf16 v[42:45], v[178:181], v[186:189], v[42:45]
	v_mfma_f32_16x16x32_bf16 v[34:37], v[170:173], v[194:197], v[34:37]
	v_mfma_f32_16x16x32_bf16 v[26:29], v[178:181], v[194:197], v[26:29]
	v_mfma_f32_16x16x32_bf16 v[18:21], v[170:173], v[202:205], v[18:21]
	v_mfma_f32_16x16x32_bf16 v[10:13], v[178:181], v[202:205], v[10:13]
	v_mfma_f32_16x16x32_bf16 v[6:9], v[170:173], v[210:213], v[6:9]
	v_mfma_f32_16x16x32_bf16 v[2:5], v[178:181], v[210:213], v[2:5]
	s_barrier
	s_add_i32 s81, 0, 0x18000
	v_add_u32_e32 v161, s81, v156
	s_add_i32 s82, 0, 0x1c000
	ds_read_b128 v[144:147], v161
	ds_read_b128 v[148:151], v161 offset:1024
	ds_read_b128 v[152:155], v161 offset:2048
	ds_read_b128 v[162:165], v161 offset:3072
	v_add_u32_e32 v161, s82, v156
	ds_read_b128 v[166:169], v161
	ds_read_b128 v[170:173], v161 offset:1024
	ds_read_b128 v[174:177], v161 offset:2048
	ds_read_b128 v[178:181], v161 offset:3072
	s_add_u32 s26, s60, 0x80000
	s_addc_u32 s27, s61, 0
	s_mov_b32 m0, s65
	v_lshl_add_u64 v[222:223], s[26:27], 0, v[132:133]
	ds_read_b128 v[182:185], v160 offset:32768
	ds_read_b128 v[186:189], v160 offset:33792
	ds_read_b128 v[190:193], v160 offset:34816
	ds_read_b128 v[194:197], v160 offset:35840
	ds_read_b128 v[198:201], v160 offset:36864
	ds_read_b128 v[202:205], v160 offset:37888
	ds_read_b128 v[206:209], v160 offset:38912
	ds_read_b128 v[210:213], v160 offset:39936
	global_load_lds_dwordx4 v[222:223], off
	v_lshl_add_u64 v[222:223], s[26:27], 0, v[134:135]
	s_mov_b32 m0, s66
	s_nop 0
	global_load_lds_dwordx4 v[222:223], off
	s_waitcnt vmcnt(8)
	s_waitcnt lgkmcnt(0)
	s_barrier
	s_waitcnt lgkmcnt(0)
	v_mfma_f32_16x16x32_bf16 v[126:129], v[144:147], v[182:185], v[126:129]
	v_mfma_f32_16x16x32_bf16 v[122:125], v[152:155], v[182:185], v[122:125]
	v_lshl_add_u64 v[242:243], v[240:241], 0, s[14:15]
	v_mfma_f32_16x16x32_bf16 v[118:121], v[144:147], v[190:193], v[118:121]
	v_mfma_f32_16x16x32_bf16 v[114:117], v[152:155], v[190:193], v[114:117]
	v_lshl_add_u64 v[244:245], v[240:241], 0, s[16:17]
	v_mfma_f32_16x16x32_bf16 v[106:109], v[144:147], v[198:201], v[106:109]
	v_mfma_f32_16x16x32_bf16 v[98:101], v[152:155], v[198:201], v[98:101]
	v_lshl_add_u64 v[248:249], v[240:241], 0, s[20:21]
	v_mfma_f32_16x16x32_bf16 v[90:93], v[144:147], v[206:209], v[90:93]
	v_mfma_f32_16x16x32_bf16 v[82:85], v[152:155], v[206:209], v[82:85]
	v_lshl_add_u64 v[240:241], v[240:241], 0, s[22:23]
	v_mfma_f32_16x16x32_bf16 v[126:129], v[148:151], v[186:189], v[126:129]
	v_mfma_f32_16x16x32_bf16 v[122:125], v[162:165], v[186:189], v[122:125]
	v_lshl_add_u64 v[250:251], v[250:251], 0, s[18:19]
	v_mfma_f32_16x16x32_bf16 v[118:121], v[148:151], v[194:197], v[118:121]
	v_mfma_f32_16x16x32_bf16 v[114:117], v[162:165], v[194:197], v[114:117]
	v_lshl_add_u64 v[246:247], v[246:247], 0, s[18:19]
	v_mfma_f32_16x16x32_bf16 v[106:109], v[148:151], v[202:205], v[106:109]
	v_mfma_f32_16x16x32_bf16 v[98:101], v[162:165], v[202:205], v[98:101]
	v_mfma_f32_16x16x32_bf16 v[90:93], v[148:151], v[210:213], v[90:93]
	v_mfma_f32_16x16x32_bf16 v[82:85], v[162:165], v[210:213], v[82:85]
	v_mfma_f32_16x16x32_bf16 v[110:113], v[166:169], v[182:185], v[110:113]
	v_mfma_f32_16x16x32_bf16 v[102:105], v[174:177], v[182:185], v[102:105]
	v_mfma_f32_16x16x32_bf16 v[94:97], v[166:169], v[190:193], v[94:97]
	v_mfma_f32_16x16x32_bf16 v[86:89], v[174:177], v[190:193], v[86:89]
	v_mfma_f32_16x16x32_bf16 v[78:81], v[166:169], v[198:201], v[78:81]
	v_mfma_f32_16x16x32_bf16 v[74:77], v[174:177], v[198:201], v[74:77]
	v_mfma_f32_16x16x32_bf16 v[70:73], v[166:169], v[206:209], v[70:73]
	v_mfma_f32_16x16x32_bf16 v[66:69], v[174:177], v[206:209], v[66:69]
	v_mfma_f32_16x16x32_bf16 v[110:113], v[170:173], v[186:189], v[110:113]
	v_mfma_f32_16x16x32_bf16 v[102:105], v[178:181], v[186:189], v[102:105]
	v_mfma_f32_16x16x32_bf16 v[94:97], v[170:173], v[194:197], v[94:97]
	v_mfma_f32_16x16x32_bf16 v[86:89], v[178:181], v[194:197], v[86:89]
	v_mfma_f32_16x16x32_bf16 v[78:81], v[170:173], v[202:205], v[78:81]
	v_mfma_f32_16x16x32_bf16 v[74:77], v[178:181], v[202:205], v[74:77]
	v_mfma_f32_16x16x32_bf16 v[70:73], v[170:173], v[210:213], v[70:73]
	v_mfma_f32_16x16x32_bf16 v[66:69], v[178:181], v[210:213], v[66:69]
	s_barrier
	s_add_i32 s26, s81, s35
	s_mov_b32 m0, s26
	ds_read_b128 v[182:185], v160 offset:49152
	ds_read_b128 v[186:189], v160 offset:50176
	ds_read_b128 v[190:193], v160 offset:51200
	ds_read_b128 v[194:197], v160 offset:52224
	ds_read_b128 v[198:201], v160 offset:53248
	ds_read_b128 v[202:205], v160 offset:54272
	ds_read_b128 v[206:209], v160 offset:55296
	ds_read_b128 v[210:213], v160 offset:56320
	global_load_lds_dwordx4 v[242:243], off
	s_add_i32 m0, s26, 0x2000
	s_add_i32 s26, s82, s35
	global_load_lds_dwordx4 v[244:245], off
	s_mov_b32 m0, s26
	s_nop 0
	global_load_lds_dwordx4 v[248:249], off
	s_add_i32 m0, s26, 0x2000
	s_nop 0
	global_load_lds_dwordx4 v[240:241], off
	s_mov_b32 m0, s68
	s_nop 0
	global_load_lds_dwordx4 v[250:251], off
	s_mov_b32 m0, s69
	s_nop 0
	global_load_lds_dwordx4 v[246:247], off
	s_waitcnt vmcnt(8)
	s_waitcnt lgkmcnt(0)
	s_barrier
	s_waitcnt lgkmcnt(0)
	v_mfma_f32_16x16x32_bf16 v[62:65], v[144:147], v[182:185], v[62:65]
	v_mfma_f32_16x16x32_bf16 v[58:61], v[152:155], v[182:185], v[58:61]
	v_mfma_f32_16x16x32_bf16 v[54:57], v[144:147], v[190:193], v[54:57]
	v_mfma_f32_16x16x32_bf16 v[46:49], v[152:155], v[190:193], v[46:49]
	v_mfma_f32_16x16x32_bf16 v[38:41], v[144:147], v[198:201], v[38:41]
	v_mfma_f32_16x16x32_bf16 v[30:33], v[152:155], v[198:201], v[30:33]
	v_mfma_f32_16x16x32_bf16 v[22:25], v[144:147], v[206:209], v[22:25]
	v_mfma_f32_16x16x32_bf16 v[14:17], v[152:155], v[206:209], v[14:17]
	v_mfma_f32_16x16x32_bf16 v[62:65], v[148:151], v[186:189], v[62:65]
	v_mfma_f32_16x16x32_bf16 v[58:61], v[162:165], v[186:189], v[58:61]
	v_mfma_f32_16x16x32_bf16 v[54:57], v[148:151], v[194:197], v[54:57]
	v_mfma_f32_16x16x32_bf16 v[46:49], v[162:165], v[194:197], v[46:49]
	v_mfma_f32_16x16x32_bf16 v[38:41], v[148:151], v[202:205], v[38:41]
	v_mfma_f32_16x16x32_bf16 v[30:33], v[162:165], v[202:205], v[30:33]
	v_mfma_f32_16x16x32_bf16 v[22:25], v[148:151], v[210:213], v[22:25]
	v_mfma_f32_16x16x32_bf16 v[14:17], v[162:165], v[210:213], v[14:17]
	v_mfma_f32_16x16x32_bf16 v[50:53], v[166:169], v[182:185], v[50:53]
	v_mfma_f32_16x16x32_bf16 v[42:45], v[174:177], v[182:185], v[42:45]
	v_mfma_f32_16x16x32_bf16 v[34:37], v[166:169], v[190:193], v[34:37]
	v_mfma_f32_16x16x32_bf16 v[26:29], v[174:177], v[190:193], v[26:29]
	v_mfma_f32_16x16x32_bf16 v[18:21], v[166:169], v[198:201], v[18:21]
	v_mfma_f32_16x16x32_bf16 v[10:13], v[174:177], v[198:201], v[10:13]
	v_mfma_f32_16x16x32_bf16 v[6:9], v[166:169], v[206:209], v[6:9]
	v_mfma_f32_16x16x32_bf16 v[2:5], v[174:177], v[206:209], v[2:5]
	v_mfma_f32_16x16x32_bf16 v[50:53], v[170:173], v[186:189], v[50:53]
	v_mfma_f32_16x16x32_bf16 v[42:45], v[178:181], v[186:189], v[42:45]
	v_mfma_f32_16x16x32_bf16 v[34:37], v[170:173], v[194:197], v[34:37]
	v_mfma_f32_16x16x32_bf16 v[26:29], v[178:181], v[194:197], v[26:29]
	v_mfma_f32_16x16x32_bf16 v[18:21], v[170:173], v[202:205], v[18:21]
	v_mfma_f32_16x16x32_bf16 v[10:13], v[178:181], v[202:205], v[10:13]
	v_mfma_f32_16x16x32_bf16 v[6:9], v[170:173], v[210:213], v[6:9]
	v_mfma_f32_16x16x32_bf16 v[2:5], v[178:181], v[210:213], v[2:5]
	s_barrier
	s_add_i32 s80, s80, 2
	s_add_u32 s74, s74, 0x10000
	s_addc_u32 s75, s75, 0
	s_add_u32 s58, s58, 0x100
	s_addc_u32 s59, s59, 0
	s_cmp_gt_u32 s80, 29
	s_cbranch_scc0 .LBB0_1271
	s_and_b64 vcc, exec, s[24:25]
	s_cbranch_vccz .LBB0_1274
	s_barrier

.LBB0_1497:
	ds_read_b128 v[26:29], v186
	ds_read_b128 v[30:33], v186 offset:1024
	ds_read_b128 v[18:21], v186 offset:2048
	ds_read_b128 v[22:25], v186 offset:3072
	ds_read_b128 v[10:13], v187
	ds_read_b128 v[14:17], v187 offset:1024
	ds_read_b128 v[2:5], v187 offset:2048
	ds_read_b128 v[6:9], v187 offset:3072
	s_add_u32 s56, s4, 0xfffc0080
	s_addc_u32 s57, s5, -1
	s_cmp_eq_u32 s49, 12
	s_cselect_b64 vcc, -1, 0
	s_cselect_b32 s57, s2, s57
	s_cselect_b32 s56, s47, s56
	v_cndmask_b32_e32 v179, v177, v175, vcc
	v_cndmask_b32_e32 v178, v176, v174, vcc
	v_lshl_add_u64 v[180:181], s[4:5], 0, v[168:169]
	s_add_i32 m0, s62, 0xc000
	ds_read_b128 v[192:195], v188
	ds_read_b128 v[196:199], v188 offset:1024
	ds_read_b128 v[200:203], v188 offset:2048
	ds_read_b128 v[204:207], v188 offset:3072
	ds_read_b128 v[208:211], v188 offset:4096
	ds_read_b128 v[212:215], v188 offset:5120
	ds_read_b128 v[220:223], v188 offset:6144
	ds_read_b128 v[224:227], v188 offset:7168
	global_load_lds_dwordx4 v[180:181], off
	v_lshl_add_u64 v[180:181], s[4:5], 0, v[170:171]
	s_add_i32 m0, s62, 0xe000
	s_nop 0
	global_load_lds_dwordx4 v[180:181], off
	s_waitcnt vmcnt(8)
	s_waitcnt lgkmcnt(0)
	s_barrier
	s_waitcnt lgkmcnt(0)
	v_mfma_scale_f32_16x16x128_f8f6f4 v[158:161], v[26:33], v[192:199], v[158:161], v189, v190 op_sel_hi:[0,0,0]
	v_mfma_scale_f32_16x16x128_f8f6f4 v[150:153], v[18:25], v[192:199], v[150:153], v189, v190 op_sel_hi:[0,0,0]
	v_lshl_add_u64 v[240:241], v[178:179], 0, v[162:163]
	v_mfma_scale_f32_16x16x128_f8f6f4 v[142:145], v[26:33], v[200:207], v[142:145], v189, v190 op_sel_hi:[0,0,0]
	v_mfma_scale_f32_16x16x128_f8f6f4 v[134:137], v[18:25], v[200:207], v[134:137], v189, v190 op_sel_hi:[0,0,0]
	v_lshl_add_u64 v[242:243], v[240:241], 0, s[10:11]
	v_mfma_scale_f32_16x16x128_f8f6f4 v[126:129], v[26:33], v[208:215], v[126:129], v189, v190 op_sel_hi:[0,0,0]
	v_mfma_scale_f32_16x16x128_f8f6f4 v[118:121], v[18:25], v[208:215], v[118:121], v189, v190 op_sel_hi:[0,0,0]
	v_lshl_add_u64 v[244:245], v[240:241], 0, s[12:13]
	v_mfma_scale_f32_16x16x128_f8f6f4 v[110:113], v[26:33], v[220:227], v[110:113], v189, v190 op_sel_hi:[0,0,0]
	v_mfma_scale_f32_16x16x128_f8f6f4 v[102:105], v[18:25], v[220:227], v[102:105], v189, v190 op_sel_hi:[0,0,0]
	v_lshl_add_u64 v[246:247], s[56:57], 0, v[166:167]
	v_mfma_scale_f32_16x16x128_f8f6f4 v[154:157], v[10:17], v[192:199], v[154:157], v189, v190 op_sel_hi:[0,0,0]
	v_mfma_scale_f32_16x16x128_f8f6f4 v[146:149], v[2:9], v[192:199], v[146:149], v189, v190 op_sel_hi:[0,0,0]
	v_lshl_add_u64 v[248:249], v[240:241], 0, s[14:15]
	v_mfma_scale_f32_16x16x128_f8f6f4 v[138:141], v[10:17], v[200:207], v[138:141], v189, v190 op_sel_hi:[0,0,0]
	v_mfma_scale_f32_16x16x128_f8f6f4 v[130:133], v[2:9], v[200:207], v[130:133], v189, v190 op_sel_hi:[0,0,0]
	v_lshl_add_u64 v[250:251], s[56:57], 0, v[164:165]
	v_mfma_scale_f32_16x16x128_f8f6f4 v[122:125], v[10:17], v[208:215], v[122:125], v189, v190 op_sel_hi:[0,0,0]
	v_mfma_scale_f32_16x16x128_f8f6f4 v[114:117], v[2:9], v[208:215], v[114:117], v189, v190 op_sel_hi:[0,0,0]
	v_mfma_scale_f32_16x16x128_f8f6f4 v[106:109], v[10:17], v[220:227], v[106:109], v189, v190 op_sel_hi:[0,0,0]
	v_mfma_scale_f32_16x16x128_f8f6f4 v[98:101], v[2:9], v[220:227], v[98:101], v189, v190 op_sel_hi:[0,0,0]
	s_barrier
	s_add_i32 s73, s69, s61
	s_mov_b32 m0, s73
	ds_read_b128 v[192:195], v188 offset:16384
	ds_read_b128 v[196:199], v188 offset:17408
	ds_read_b128 v[200:203], v188 offset:18432
	ds_read_b128 v[204:207], v188 offset:19456
	ds_read_b128 v[208:211], v188 offset:20480
	ds_read_b128 v[212:215], v188 offset:21504
	ds_read_b128 v[220:223], v188 offset:22528
	ds_read_b128 v[224:227], v188 offset:23552
	global_load_lds_dwordx4 v[240:241], off
	s_add_i32 m0, s73, 0x2000
	s_add_i32 s73, s70, s61
	global_load_lds_dwordx4 v[242:243], off
	s_mov_b32 m0, s73
	s_nop 0
	global_load_lds_dwordx4 v[244:245], off
	s_add_i32 m0, s73, 0x2000
	s_nop 0
	global_load_lds_dwordx4 v[248:249], off
	s_mov_b32 m0, s62
	s_nop 0
	global_load_lds_dwordx4 v[250:251], off
	s_mov_b32 m0, s53
	s_nop 0
	global_load_lds_dwordx4 v[246:247], off
	s_waitcnt vmcnt(8)
	s_waitcnt lgkmcnt(0)
	s_barrier
	s_waitcnt lgkmcnt(0)
	v_mfma_scale_f32_16x16x128_f8f6f4 v[94:97], v[26:33], v[192:199], v[94:97], v189, v190 op_sel_hi:[0,0,0]
	v_mfma_scale_f32_16x16x128_f8f6f4 v[86:89], v[18:25], v[192:199], v[86:89], v189, v190 op_sel_hi:[0,0,0]
	v_mfma_scale_f32_16x16x128_f8f6f4 v[78:81], v[26:33], v[200:207], v[78:81], v189, v190 op_sel_hi:[0,0,0]
	v_mfma_scale_f32_16x16x128_f8f6f4 v[70:73], v[18:25], v[200:207], v[70:73], v189, v190 op_sel_hi:[0,0,0]
	v_mfma_scale_f32_16x16x128_f8f6f4 v[62:65], v[26:33], v[208:215], v[62:65], v189, v190 op_sel_hi:[0,0,0]
	v_mfma_scale_f32_16x16x128_f8f6f4 v[54:57], v[18:25], v[208:215], v[54:57], v189, v190 op_sel_hi:[0,0,0]
	v_mfma_scale_f32_16x16x128_f8f6f4 v[46:49], v[26:33], v[220:227], v[46:49], v189, v190 op_sel_hi:[0,0,0]
	v_mfma_scale_f32_16x16x128_f8f6f4 v[38:41], v[18:25], v[220:227], v[38:41], v189, v190 op_sel_hi:[0,0,0]
	v_mfma_scale_f32_16x16x128_f8f6f4 v[90:93], v[10:17], v[192:199], v[90:93], v189, v190 op_sel_hi:[0,0,0]
	v_mfma_scale_f32_16x16x128_f8f6f4 v[82:85], v[2:9], v[192:199], v[82:85], v189, v190 op_sel_hi:[0,0,0]
	v_mfma_scale_f32_16x16x128_f8f6f4 v[74:77], v[10:17], v[200:207], v[74:77], v189, v190 op_sel_hi:[0,0,0]
	v_mfma_scale_f32_16x16x128_f8f6f4 v[66:69], v[2:9], v[200:207], v[66:69], v189, v190 op_sel_hi:[0,0,0]
	v_mfma_scale_f32_16x16x128_f8f6f4 v[58:61], v[10:17], v[208:215], v[58:61], v189, v190 op_sel_hi:[0,0,0]
	v_mfma_scale_f32_16x16x128_f8f6f4 v[50:53], v[2:9], v[208:215], v[50:53], v189, v190 op_sel_hi:[0,0,0]
	v_mfma_scale_f32_16x16x128_f8f6f4 v[42:45], v[10:17], v[220:227], v[42:45], v189, v190 op_sel_hi:[0,0,0]
	v_mfma_scale_f32_16x16x128_f8f6f4 v[34:37], v[2:9], v[220:227], v[34:37], v189, v190 op_sel_hi:[0,0,0]
	s_barrier
	s_add_i32 s73, 0, 0x18000
	s_add_i32 s74, 0, 0x1c000
	v_add_u32_e32 v14, s73, v184
	v_add_u32_e32 v30, s74, v184
	ds_read_b128 v[2:5], v14
	ds_read_b128 v[6:9], v14 offset:1024
	ds_read_b128 v[10:13], v14 offset:2048
	ds_read_b128 v[14:17], v14 offset:3072
	ds_read_b128 v[18:21], v30
	ds_read_b128 v[22:25], v30 offset:1024
	ds_read_b128 v[26:29], v30 offset:2048
	ds_read_b128 v[30:33], v30 offset:3072
	s_add_u32 s56, s56, 0x40000
	s_addc_u32 s57, s57, 0
	s_mov_b32 m0, s63
	v_lshl_add_u64 v[216:217], s[56:57], 0, v[164:165]
	ds_read_b128 v[192:195], v188 offset:32768
	ds_read_b128 v[196:199], v188 offset:33792
	ds_read_b128 v[200:203], v188 offset:34816
	ds_read_b128 v[204:207], v188 offset:35840
	ds_read_b128 v[208:211], v188 offset:36864
	ds_read_b128 v[212:215], v188 offset:37888
	ds_read_b128 v[220:223], v188 offset:38912
	ds_read_b128 v[224:227], v188 offset:39936
	global_load_lds_dwordx4 v[216:217], off
	v_lshl_add_u64 v[216:217], s[56:57], 0, v[166:167]
	s_mov_b32 m0, s64
	s_nop 0
	global_load_lds_dwordx4 v[216:217], off
	s_waitcnt vmcnt(8)
	s_waitcnt lgkmcnt(0)
	s_barrier
	s_waitcnt lgkmcnt(0)
	v_mfma_scale_f32_16x16x128_f8f6f4 v[158:161], v[2:9], v[192:199], v[158:161], v189, v190 op_sel_hi:[0,0,0]
	v_mfma_scale_f32_16x16x128_f8f6f4 v[150:153], v[10:17], v[192:199], v[150:153], v189, v190 op_sel_hi:[0,0,0]
	v_lshl_add_u64 v[242:243], v[240:241], 0, s[20:21]
	v_mfma_scale_f32_16x16x128_f8f6f4 v[142:145], v[2:9], v[200:207], v[142:145], v189, v190 op_sel_hi:[0,0,0]
	v_mfma_scale_f32_16x16x128_f8f6f4 v[134:137], v[10:17], v[200:207], v[134:137], v189, v190 op_sel_hi:[0,0,0]
	v_lshl_add_u64 v[244:245], v[240:241], 0, s[22:23]
	v_mfma_scale_f32_16x16x128_f8f6f4 v[126:129], v[2:9], v[208:215], v[126:129], v189, v190 op_sel_hi:[0,0,0]
	v_mfma_scale_f32_16x16x128_f8f6f4 v[118:121], v[10:17], v[208:215], v[118:121], v189, v190 op_sel_hi:[0,0,0]
	v_lshl_add_u64 v[248:249], v[240:241], 0, s[26:27]
	v_mfma_scale_f32_16x16x128_f8f6f4 v[110:113], v[2:9], v[220:227], v[110:113], v189, v190 op_sel_hi:[0,0,0]
	v_mfma_scale_f32_16x16x128_f8f6f4 v[102:105], v[10:17], v[220:227], v[102:105], v189, v190 op_sel_hi:[0,0,0]
	v_lshl_add_u64 v[240:241], v[240:241], 0, s[36:37]
	v_mfma_scale_f32_16x16x128_f8f6f4 v[154:157], v[18:25], v[192:199], v[154:157], v189, v190 op_sel_hi:[0,0,0]
	v_mfma_scale_f32_16x16x128_f8f6f4 v[146:149], v[26:33], v[192:199], v[146:149], v189, v190 op_sel_hi:[0,0,0]
	v_lshl_add_u64 v[250:251], v[250:251], 0, s[24:25]
	v_mfma_scale_f32_16x16x128_f8f6f4 v[138:141], v[18:25], v[200:207], v[138:141], v189, v190 op_sel_hi:[0,0,0]
	v_mfma_scale_f32_16x16x128_f8f6f4 v[130:133], v[26:33], v[200:207], v[130:133], v189, v190 op_sel_hi:[0,0,0]
	v_lshl_add_u64 v[246:247], v[246:247], 0, s[24:25]
	v_mfma_scale_f32_16x16x128_f8f6f4 v[122:125], v[18:25], v[208:215], v[122:125], v189, v190 op_sel_hi:[0,0,0]
	v_mfma_scale_f32_16x16x128_f8f6f4 v[114:117], v[26:33], v[208:215], v[114:117], v189, v190 op_sel_hi:[0,0,0]
	v_mfma_scale_f32_16x16x128_f8f6f4 v[106:109], v[18:25], v[220:227], v[106:109], v189, v190 op_sel_hi:[0,0,0]
	v_mfma_scale_f32_16x16x128_f8f6f4 v[98:101], v[26:33], v[220:227], v[98:101], v189, v190 op_sel_hi:[0,0,0]
	s_barrier
	s_add_i32 s56, s73, s61
	s_mov_b32 m0, s56
	ds_read_b128 v[192:195], v188 offset:49152
	ds_read_b128 v[196:199], v188 offset:50176
	ds_read_b128 v[200:203], v188 offset:51200
	ds_read_b128 v[204:207], v188 offset:52224
	ds_read_b128 v[208:211], v188 offset:53248
	ds_read_b128 v[212:215], v188 offset:54272
	ds_read_b128 v[220:223], v188 offset:55296
	ds_read_b128 v[224:227], v188 offset:56320
	global_load_lds_dwordx4 v[242:243], off
	s_add_i32 m0, s56, 0x2000
	s_add_i32 s56, s74, s61
	global_load_lds_dwordx4 v[244:245], off
	s_mov_b32 m0, s56
	s_nop 0
	global_load_lds_dwordx4 v[248:249], off
	s_add_i32 m0, s56, 0x2000
	s_nop 0
	global_load_lds_dwordx4 v[240:241], off
	s_mov_b32 m0, s66
	s_nop 0
	global_load_lds_dwordx4 v[250:251], off
	s_mov_b32 m0, s67
	s_nop 0
	global_load_lds_dwordx4 v[246:247], off
	s_waitcnt vmcnt(8)
	s_waitcnt lgkmcnt(0)
	s_barrier
	s_waitcnt lgkmcnt(0)
	v_mfma_scale_f32_16x16x128_f8f6f4 v[94:97], v[2:9], v[192:199], v[94:97], v189, v190 op_sel_hi:[0,0,0]
	v_mfma_scale_f32_16x16x128_f8f6f4 v[86:89], v[10:17], v[192:199], v[86:89], v189, v190 op_sel_hi:[0,0,0]
	v_mfma_scale_f32_16x16x128_f8f6f4 v[78:81], v[2:9], v[200:207], v[78:81], v189, v190 op_sel_hi:[0,0,0]
	v_mfma_scale_f32_16x16x128_f8f6f4 v[70:73], v[10:17], v[200:207], v[70:73], v189, v190 op_sel_hi:[0,0,0]
	v_mfma_scale_f32_16x16x128_f8f6f4 v[62:65], v[2:9], v[208:215], v[62:65], v189, v190 op_sel_hi:[0,0,0]
	v_mfma_scale_f32_16x16x128_f8f6f4 v[54:57], v[10:17], v[208:215], v[54:57], v189, v190 op_sel_hi:[0,0,0]
	v_mfma_scale_f32_16x16x128_f8f6f4 v[46:49], v[2:9], v[220:227], v[46:49], v189, v190 op_sel_hi:[0,0,0]
	v_mfma_scale_f32_16x16x128_f8f6f4 v[38:41], v[10:17], v[220:227], v[38:41], v189, v190 op_sel_hi:[0,0,0]
	v_mfma_scale_f32_16x16x128_f8f6f4 v[90:93], v[18:25], v[192:199], v[90:93], v189, v190 op_sel_hi:[0,0,0]
	v_mfma_scale_f32_16x16x128_f8f6f4 v[82:85], v[26:33], v[192:199], v[82:85], v189, v190 op_sel_hi:[0,0,0]
	v_mfma_scale_f32_16x16x128_f8f6f4 v[74:77], v[18:25], v[200:207], v[74:77], v189, v190 op_sel_hi:[0,0,0]
	v_mfma_scale_f32_16x16x128_f8f6f4 v[66:69], v[26:33], v[200:207], v[66:69], v189, v190 op_sel_hi:[0,0,0]
	v_mfma_scale_f32_16x16x128_f8f6f4 v[58:61], v[18:25], v[208:215], v[58:61], v189, v190 op_sel_hi:[0,0,0]
	v_mfma_scale_f32_16x16x128_f8f6f4 v[50:53], v[26:33], v[208:215], v[50:53], v189, v190 op_sel_hi:[0,0,0]
	v_mfma_scale_f32_16x16x128_f8f6f4 v[42:45], v[18:25], v[220:227], v[42:45], v189, v190 op_sel_hi:[0,0,0]
	v_mfma_scale_f32_16x16x128_f8f6f4 v[34:37], v[26:33], v[220:227], v[34:37], v189, v190 op_sel_hi:[0,0,0]
	s_barrier
	s_add_i32 s49, s49, 2
	s_add_u32 s4, s4, 0x100
	s_addc_u32 s5, s5, 0
	s_cmp_gt_u32 s49, 13
	v_lshl_add_u64 v[176:177], v[176:177], 0, s[40:41]
	s_cbranch_scc0 .LBB0_1497
	s_and_b64 vcc, exec, s[38:39]
	s_cbranch_vccz .LBB0_1500
	s_barrier

.LBB0_1568:
	ds_read_b128 v[26:29], v186
	ds_read_b128 v[30:33], v186 offset:1024
	ds_read_b128 v[18:21], v186 offset:2048
	ds_read_b128 v[22:25], v186 offset:3072
	ds_read_b128 v[10:13], v187
	ds_read_b128 v[14:17], v187 offset:1024
	ds_read_b128 v[2:5], v187 offset:2048
	ds_read_b128 v[6:9], v187 offset:3072
	s_add_u32 s58, s56, 0xfff50080
	s_addc_u32 s59, s57, -1
	s_cmp_eq_u32 s53, 40
	s_cselect_b64 vcc, -1, 0
	s_cselect_b32 s59, s5, s59
	s_cselect_b32 s58, s4, s58
	v_cndmask_b32_e32 v179, v177, v175, vcc
	v_cndmask_b32_e32 v178, v176, v174, vcc
	v_lshl_add_u64 v[180:181], s[56:57], 0, v[170:171]
	s_add_i32 m0, s61, 0xc000
	ds_read_b128 v[192:195], v188
	ds_read_b128 v[196:199], v188 offset:1024
	ds_read_b128 v[200:203], v188 offset:2048
	ds_read_b128 v[204:207], v188 offset:3072
	ds_read_b128 v[208:211], v188 offset:4096
	ds_read_b128 v[212:215], v188 offset:5120
	ds_read_b128 v[220:223], v188 offset:6144
	ds_read_b128 v[224:227], v188 offset:7168
	global_load_lds_dwordx4 v[180:181], off
	v_lshl_add_u64 v[180:181], s[56:57], 0, v[172:173]
	s_add_i32 m0, s61, 0xe000
	s_nop 0
	global_load_lds_dwordx4 v[180:181], off
	s_waitcnt vmcnt(8)
	s_waitcnt lgkmcnt(0)
	s_barrier
	s_waitcnt lgkmcnt(0)
	v_mfma_scale_f32_16x16x128_f8f6f4 v[158:161], v[26:33], v[192:199], v[158:161], v189, v190 op_sel_hi:[0,0,0]
	v_mfma_scale_f32_16x16x128_f8f6f4 v[154:157], v[18:25], v[192:199], v[154:157], v189, v190 op_sel_hi:[0,0,0]
	v_lshl_add_u64 v[240:241], v[178:179], 0, v[164:165]
	v_mfma_scale_f32_16x16x128_f8f6f4 v[150:153], v[26:33], v[200:207], v[150:153], v189, v190 op_sel_hi:[0,0,0]
	v_mfma_scale_f32_16x16x128_f8f6f4 v[142:145], v[18:25], v[200:207], v[142:145], v189, v190 op_sel_hi:[0,0,0]
	v_lshl_add_u64 v[242:243], v[240:241], 0, s[10:11]
	v_mfma_scale_f32_16x16x128_f8f6f4 v[134:137], v[26:33], v[208:215], v[134:137], v189, v190 op_sel_hi:[0,0,0]
	v_mfma_scale_f32_16x16x128_f8f6f4 v[126:129], v[18:25], v[208:215], v[126:129], v189, v190 op_sel_hi:[0,0,0]
	v_lshl_add_u64 v[244:245], v[240:241], 0, s[12:13]
	v_mfma_scale_f32_16x16x128_f8f6f4 v[118:121], v[26:33], v[220:227], v[118:121], v189, v190 op_sel_hi:[0,0,0]
	v_mfma_scale_f32_16x16x128_f8f6f4 v[110:113], v[18:25], v[220:227], v[110:113], v189, v190 op_sel_hi:[0,0,0]
	v_lshl_add_u64 v[246:247], s[58:59], 0, v[168:169]
	v_mfma_scale_f32_16x16x128_f8f6f4 v[146:149], v[10:17], v[192:199], v[146:149], v189, v190 op_sel_hi:[0,0,0]
	v_mfma_scale_f32_16x16x128_f8f6f4 v[138:141], v[2:9], v[192:199], v[138:141], v189, v190 op_sel_hi:[0,0,0]
	v_lshl_add_u64 v[248:249], v[240:241], 0, s[14:15]
	v_mfma_scale_f32_16x16x128_f8f6f4 v[130:133], v[10:17], v[200:207], v[130:133], v189, v190 op_sel_hi:[0,0,0]
	v_mfma_scale_f32_16x16x128_f8f6f4 v[122:125], v[2:9], v[200:207], v[122:125], v189, v190 op_sel_hi:[0,0,0]
	v_lshl_add_u64 v[250:251], s[58:59], 0, v[166:167]
	v_mfma_scale_f32_16x16x128_f8f6f4 v[114:117], v[10:17], v[208:215], v[114:117], v189, v190 op_sel_hi:[0,0,0]
	v_mfma_scale_f32_16x16x128_f8f6f4 v[106:109], v[2:9], v[208:215], v[106:109], v189, v190 op_sel_hi:[0,0,0]
	v_mfma_scale_f32_16x16x128_f8f6f4 v[102:105], v[10:17], v[220:227], v[102:105], v189, v190 op_sel_hi:[0,0,0]
	v_mfma_scale_f32_16x16x128_f8f6f4 v[98:101], v[2:9], v[220:227], v[98:101], v189, v190 op_sel_hi:[0,0,0]
	s_barrier
	s_add_i32 s80, s69, s33
	s_mov_b32 m0, s80
	ds_read_b128 v[192:195], v188 offset:16384
	ds_read_b128 v[196:199], v188 offset:17408
	ds_read_b128 v[200:203], v188 offset:18432
	ds_read_b128 v[204:207], v188 offset:19456
	ds_read_b128 v[208:211], v188 offset:20480
	ds_read_b128 v[212:215], v188 offset:21504
	ds_read_b128 v[220:223], v188 offset:22528
	ds_read_b128 v[224:227], v188 offset:23552
	global_load_lds_dwordx4 v[240:241], off
	s_add_i32 m0, s80, 0x2000
	s_add_i32 s80, s70, s33
	global_load_lds_dwordx4 v[242:243], off
	s_mov_b32 m0, s80
	s_nop 0
	global_load_lds_dwordx4 v[244:245], off
	s_add_i32 m0, s80, 0x2000
	s_nop 0
	global_load_lds_dwordx4 v[248:249], off
	s_mov_b32 m0, s61
	s_nop 0
	global_load_lds_dwordx4 v[250:251], off
	s_mov_b32 m0, s62
	s_nop 0
	global_load_lds_dwordx4 v[246:247], off
	s_waitcnt vmcnt(8)
	s_waitcnt lgkmcnt(0)
	s_barrier
	s_waitcnt lgkmcnt(0)
	v_mfma_scale_f32_16x16x128_f8f6f4 v[94:97], v[26:33], v[192:199], v[94:97], v189, v190 op_sel_hi:[0,0,0]
	v_mfma_scale_f32_16x16x128_f8f6f4 v[90:93], v[18:25], v[192:199], v[90:93], v189, v190 op_sel_hi:[0,0,0]
	v_mfma_scale_f32_16x16x128_f8f6f4 v[86:89], v[26:33], v[200:207], v[86:89], v189, v190 op_sel_hi:[0,0,0]
	v_mfma_scale_f32_16x16x128_f8f6f4 v[78:81], v[18:25], v[200:207], v[78:81], v189, v190 op_sel_hi:[0,0,0]
	v_mfma_scale_f32_16x16x128_f8f6f4 v[70:73], v[26:33], v[208:215], v[70:73], v189, v190 op_sel_hi:[0,0,0]
	v_mfma_scale_f32_16x16x128_f8f6f4 v[62:65], v[18:25], v[208:215], v[62:65], v189, v190 op_sel_hi:[0,0,0]
	v_mfma_scale_f32_16x16x128_f8f6f4 v[54:57], v[26:33], v[220:227], v[54:57], v189, v190 op_sel_hi:[0,0,0]
	v_mfma_scale_f32_16x16x128_f8f6f4 v[46:49], v[18:25], v[220:227], v[46:49], v189, v190 op_sel_hi:[0,0,0]
	v_mfma_scale_f32_16x16x128_f8f6f4 v[82:85], v[10:17], v[192:199], v[82:85], v189, v190 op_sel_hi:[0,0,0]
	v_mfma_scale_f32_16x16x128_f8f6f4 v[74:77], v[2:9], v[192:199], v[74:77], v189, v190 op_sel_hi:[0,0,0]
	v_mfma_scale_f32_16x16x128_f8f6f4 v[66:69], v[10:17], v[200:207], v[66:69], v189, v190 op_sel_hi:[0,0,0]
	v_mfma_scale_f32_16x16x128_f8f6f4 v[58:61], v[2:9], v[200:207], v[58:61], v189, v190 op_sel_hi:[0,0,0]
	v_mfma_scale_f32_16x16x128_f8f6f4 v[50:53], v[10:17], v[208:215], v[50:53], v189, v190 op_sel_hi:[0,0,0]
	v_mfma_scale_f32_16x16x128_f8f6f4 v[42:45], v[2:9], v[208:215], v[42:45], v189, v190 op_sel_hi:[0,0,0]
	v_mfma_scale_f32_16x16x128_f8f6f4 v[38:41], v[10:17], v[220:227], v[38:41], v189, v190 op_sel_hi:[0,0,0]
	v_mfma_scale_f32_16x16x128_f8f6f4 v[34:37], v[2:9], v[220:227], v[34:37], v189, v190 op_sel_hi:[0,0,0]
	s_barrier
	s_add_i32 s80, 0, 0x18000
	s_add_i32 s81, 0, 0x1c000
	v_add_u32_e32 v14, s80, v184
	v_add_u32_e32 v30, s81, v184
	ds_read_b128 v[2:5], v14
	ds_read_b128 v[6:9], v14 offset:1024
	ds_read_b128 v[10:13], v14 offset:2048
	ds_read_b128 v[14:17], v14 offset:3072
	ds_read_b128 v[18:21], v30
	ds_read_b128 v[22:25], v30 offset:1024
	ds_read_b128 v[26:29], v30 offset:2048
	ds_read_b128 v[30:33], v30 offset:3072
	s_add_u32 s58, s58, 0xb0000
	s_addc_u32 s59, s59, 0
	s_mov_b32 m0, s63
	v_lshl_add_u64 v[216:217], s[58:59], 0, v[166:167]
	ds_read_b128 v[192:195], v188 offset:32768
	ds_read_b128 v[196:199], v188 offset:33792
	ds_read_b128 v[200:203], v188 offset:34816
	ds_read_b128 v[204:207], v188 offset:35840
	ds_read_b128 v[208:211], v188 offset:36864
	ds_read_b128 v[212:215], v188 offset:37888
	ds_read_b128 v[220:223], v188 offset:38912
	ds_read_b128 v[224:227], v188 offset:39936
	global_load_lds_dwordx4 v[216:217], off
	v_lshl_add_u64 v[216:217], s[58:59], 0, v[168:169]
	s_mov_b32 m0, s64
	s_nop 0
	global_load_lds_dwordx4 v[216:217], off
	s_waitcnt vmcnt(8)
	s_waitcnt lgkmcnt(0)
	s_barrier
	s_waitcnt lgkmcnt(0)
	v_mfma_scale_f32_16x16x128_f8f6f4 v[158:161], v[2:9], v[192:199], v[158:161], v189, v190 op_sel_hi:[0,0,0]
	v_mfma_scale_f32_16x16x128_f8f6f4 v[154:157], v[10:17], v[192:199], v[154:157], v189, v190 op_sel_hi:[0,0,0]
	v_lshl_add_u64 v[242:243], v[240:241], 0, s[24:25]
	v_mfma_scale_f32_16x16x128_f8f6f4 v[150:153], v[2:9], v[200:207], v[150:153], v189, v190 op_sel_hi:[0,0,0]
	v_mfma_scale_f32_16x16x128_f8f6f4 v[142:145], v[10:17], v[200:207], v[142:145], v189, v190 op_sel_hi:[0,0,0]
	v_lshl_add_u64 v[244:245], v[240:241], 0, s[26:27]
	v_mfma_scale_f32_16x16x128_f8f6f4 v[134:137], v[2:9], v[208:215], v[134:137], v189, v190 op_sel_hi:[0,0,0]
	v_mfma_scale_f32_16x16x128_f8f6f4 v[126:129], v[10:17], v[208:215], v[126:129], v189, v190 op_sel_hi:[0,0,0]
	v_lshl_add_u64 v[248:249], v[240:241], 0, s[38:39]
	v_mfma_scale_f32_16x16x128_f8f6f4 v[118:121], v[2:9], v[220:227], v[118:121], v189, v190 op_sel_hi:[0,0,0]
	v_mfma_scale_f32_16x16x128_f8f6f4 v[110:113], v[10:17], v[220:227], v[110:113], v189, v190 op_sel_hi:[0,0,0]
	v_lshl_add_u64 v[240:241], v[240:241], 0, s[40:41]
	v_mfma_scale_f32_16x16x128_f8f6f4 v[146:149], v[18:25], v[192:199], v[146:149], v189, v190 op_sel_hi:[0,0,0]
	v_mfma_scale_f32_16x16x128_f8f6f4 v[138:141], v[26:33], v[192:199], v[138:141], v189, v190 op_sel_hi:[0,0,0]
	v_lshl_add_u64 v[250:251], v[250:251], 0, s[36:37]
	v_mfma_scale_f32_16x16x128_f8f6f4 v[130:133], v[18:25], v[200:207], v[130:133], v189, v190 op_sel_hi:[0,0,0]
	v_mfma_scale_f32_16x16x128_f8f6f4 v[122:125], v[26:33], v[200:207], v[122:125], v189, v190 op_sel_hi:[0,0,0]
	v_lshl_add_u64 v[246:247], v[246:247], 0, s[36:37]
	v_mfma_scale_f32_16x16x128_f8f6f4 v[114:117], v[18:25], v[208:215], v[114:117], v189, v190 op_sel_hi:[0,0,0]
	v_mfma_scale_f32_16x16x128_f8f6f4 v[106:109], v[26:33], v[208:215], v[106:109], v189, v190 op_sel_hi:[0,0,0]
	v_mfma_scale_f32_16x16x128_f8f6f4 v[102:105], v[18:25], v[220:227], v[102:105], v189, v190 op_sel_hi:[0,0,0]
	v_mfma_scale_f32_16x16x128_f8f6f4 v[98:101], v[26:33], v[220:227], v[98:101], v189, v190 op_sel_hi:[0,0,0]
	s_barrier
	s_add_i32 s58, s80, s33
	s_mov_b32 m0, s58
	ds_read_b128 v[192:195], v188 offset:49152
	ds_read_b128 v[196:199], v188 offset:50176
	ds_read_b128 v[200:203], v188 offset:51200
	ds_read_b128 v[204:207], v188 offset:52224
	ds_read_b128 v[208:211], v188 offset:53248
	ds_read_b128 v[212:215], v188 offset:54272
	ds_read_b128 v[220:223], v188 offset:55296
	ds_read_b128 v[224:227], v188 offset:56320
	global_load_lds_dwordx4 v[242:243], off
	s_add_i32 m0, s58, 0x2000
	s_add_i32 s58, s81, s33
	global_load_lds_dwordx4 v[244:245], off
	s_mov_b32 m0, s58
	s_nop 0
	global_load_lds_dwordx4 v[248:249], off
	s_add_i32 m0, s58, 0x2000
	s_nop 0
	global_load_lds_dwordx4 v[240:241], off
	s_mov_b32 m0, s66
	s_nop 0
	global_load_lds_dwordx4 v[250:251], off
	s_mov_b32 m0, s67
	s_nop 0
	global_load_lds_dwordx4 v[246:247], off
	s_waitcnt vmcnt(8)
	s_waitcnt lgkmcnt(0)
	s_barrier
	s_waitcnt lgkmcnt(0)
	v_mfma_scale_f32_16x16x128_f8f6f4 v[94:97], v[2:9], v[192:199], v[94:97], v189, v190 op_sel_hi:[0,0,0]
	v_mfma_scale_f32_16x16x128_f8f6f4 v[90:93], v[10:17], v[192:199], v[90:93], v189, v190 op_sel_hi:[0,0,0]
	v_mfma_scale_f32_16x16x128_f8f6f4 v[86:89], v[2:9], v[200:207], v[86:89], v189, v190 op_sel_hi:[0,0,0]
	v_mfma_scale_f32_16x16x128_f8f6f4 v[78:81], v[10:17], v[200:207], v[78:81], v189, v190 op_sel_hi:[0,0,0]
	v_mfma_scale_f32_16x16x128_f8f6f4 v[70:73], v[2:9], v[208:215], v[70:73], v189, v190 op_sel_hi:[0,0,0]
	v_mfma_scale_f32_16x16x128_f8f6f4 v[62:65], v[10:17], v[208:215], v[62:65], v189, v190 op_sel_hi:[0,0,0]
	v_mfma_scale_f32_16x16x128_f8f6f4 v[54:57], v[2:9], v[220:227], v[54:57], v189, v190 op_sel_hi:[0,0,0]
	v_mfma_scale_f32_16x16x128_f8f6f4 v[46:49], v[10:17], v[220:227], v[46:49], v189, v190 op_sel_hi:[0,0,0]
	v_mfma_scale_f32_16x16x128_f8f6f4 v[82:85], v[18:25], v[192:199], v[82:85], v189, v190 op_sel_hi:[0,0,0]
	v_mfma_scale_f32_16x16x128_f8f6f4 v[74:77], v[26:33], v[192:199], v[74:77], v189, v190 op_sel_hi:[0,0,0]
	v_mfma_scale_f32_16x16x128_f8f6f4 v[66:69], v[18:25], v[200:207], v[66:69], v189, v190 op_sel_hi:[0,0,0]
	v_mfma_scale_f32_16x16x128_f8f6f4 v[58:61], v[26:33], v[200:207], v[58:61], v189, v190 op_sel_hi:[0,0,0]
	v_mfma_scale_f32_16x16x128_f8f6f4 v[50:53], v[18:25], v[208:215], v[50:53], v189, v190 op_sel_hi:[0,0,0]
	v_mfma_scale_f32_16x16x128_f8f6f4 v[42:45], v[26:33], v[208:215], v[42:45], v189, v190 op_sel_hi:[0,0,0]
	v_mfma_scale_f32_16x16x128_f8f6f4 v[38:41], v[18:25], v[220:227], v[38:41], v189, v190 op_sel_hi:[0,0,0]
	v_mfma_scale_f32_16x16x128_f8f6f4 v[34:37], v[26:33], v[220:227], v[34:37], v189, v190 op_sel_hi:[0,0,0]
	s_barrier
	s_add_i32 s53, s53, 2
	s_add_u32 s56, s56, 0x100
	s_addc_u32 s57, s57, 0
	s_cmp_gt_u32 s53, 41
	v_lshl_add_u64 v[176:177], v[176:177], 0, s[44:45]
	s_cbranch_scc0 .LBB0_1568
	s_and_b64 vcc, exec, s[42:43]
	s_cbranch_vccz .LBB0_1571
	s_barrier
